# P2 retention chunk loop software-pipelined: next chunk K/V/q prefetched into spare VGPRs one chunk ahead
# speedup vs baseline: 1.0132x; 1.0132x over previous
.LBB0_111:
	ds_read_b128 v[134:137], v174
	ds_read_b128 v[138:141], v174 offset:1024
	ds_read_b128 v[142:145], v174 offset:2048
	ds_read_b128 v[166:169], v174 offset:3072
	ds_read_b128 v[178:181], v175
	ds_read_b128 v[182:185], v175 offset:1024
	ds_read_b128 v[186:189], v175 offset:2048
	ds_read_b128 v[190:193], v175 offset:3072
	s_add_u32 s28, s20, s26
	s_addc_u32 s29, s21, s27
	s_add_u32 s30, s28, 0x100
	s_addc_u32 s31, s29, 0
	s_add_u32 s54, s51, s26
	s_addc_u32 s55, s52, s27
	s_cmp_eq_u32 s26, 0
	s_cselect_b64 s[28:29], -1, 0
	s_and_b64 s[28:29], s[22:23], s[28:29]
	s_cmpk_eq_i32 s26, 0x1f00
	v_cndmask_b32_e64 v170, 0, 1, s[28:29]
	s_cselect_b32 s31, s7, s31
	s_cselect_b32 s30, s15, s30
	v_readfirstlane_b32 s56, v170
	s_cselect_b32 s29, s3, s55
	s_cselect_b32 s28, s25, s54
	v_lshl_add_u64 v[170:171], v[130:131], 0, s[26:27]
	s_add_i32 m0, s39, 0xc000
	ds_read_b128 v[194:197], v176
	ds_read_b128 v[198:201], v176 offset:1024
	ds_read_b128 v[202:205], v176 offset:2048
	ds_read_b128 v[206:209], v176 offset:3072
	ds_read_b128 v[210:213], v176 offset:4096
	ds_read_b128 v[214:217], v176 offset:5120
	ds_read_b128 v[218:221], v176 offset:6144
	ds_read_b128 v[222:225], v176 offset:7168
	global_load_lds_dwordx4 v[170:171], off
	v_lshl_add_u64 v[170:171], v[132:133], 0, s[26:27]
	s_add_i32 m0, s39, 0xe000
	s_and_b32 s56, s56, 1
	global_load_lds_dwordx4 v[170:171], off
	s_cmp_lg_u32 s56, 0
	s_cbranch_scc1 .Lpg8r0
	s_waitcnt vmcnt(8)
	s_branch .Lpg8e0

.Lpg8e0:
	s_waitcnt lgkmcnt(0)
	s_barrier
	s_setprio 1
	s_waitcnt lgkmcnt(0)
	v_mfma_f32_16x16x32_bf16 v[126:129], v[134:137], v[194:197], v[126:129]
	v_mfma_f32_16x16x32_bf16 v[122:125], v[142:145], v[194:197], v[122:125]
	v_mfma_f32_16x16x32_bf16 v[110:113], v[134:137], v[202:205], v[110:113]
	v_mfma_f32_16x16x32_bf16 v[106:109], v[142:145], v[202:205], v[106:109]
	v_mfma_f32_16x16x32_bf16 v[94:97], v[134:137], v[210:213], v[94:97]
	v_mfma_f32_16x16x32_bf16 v[90:93], v[142:145], v[210:213], v[90:93]
	v_mfma_f32_16x16x32_bf16 v[78:81], v[134:137], v[218:221], v[78:81]
	v_mfma_f32_16x16x32_bf16 v[74:77], v[142:145], v[218:221], v[74:77]
	v_mfma_f32_16x16x32_bf16 v[126:129], v[138:141], v[198:201], v[126:129]
	v_mfma_f32_16x16x32_bf16 v[122:125], v[166:169], v[198:201], v[122:125]
	v_mfma_f32_16x16x32_bf16 v[110:113], v[138:141], v[206:209], v[110:113]
	v_mfma_f32_16x16x32_bf16 v[106:109], v[166:169], v[206:209], v[106:109]
	v_mfma_f32_16x16x32_bf16 v[94:97], v[138:141], v[214:217], v[94:97]
	v_mfma_f32_16x16x32_bf16 v[90:93], v[166:169], v[214:217], v[90:93]
	v_mfma_f32_16x16x32_bf16 v[78:81], v[138:141], v[222:225], v[78:81]
	v_mfma_f32_16x16x32_bf16 v[74:77], v[166:169], v[222:225], v[74:77]
	s_setprio 0
	s_setprio 1
	v_mfma_f32_16x16x32_bf16 v[118:121], v[178:181], v[194:197], v[118:121]
	v_mfma_f32_16x16x32_bf16 v[114:117], v[186:189], v[194:197], v[114:117]
	v_mfma_f32_16x16x32_bf16 v[102:105], v[178:181], v[202:205], v[102:105]
	v_mfma_f32_16x16x32_bf16 v[98:101], v[186:189], v[202:205], v[98:101]
	v_mfma_f32_16x16x32_bf16 v[86:89], v[178:181], v[210:213], v[86:89]
	v_mfma_f32_16x16x32_bf16 v[82:85], v[186:189], v[210:213], v[82:85]
	v_mfma_f32_16x16x32_bf16 v[70:73], v[178:181], v[218:221], v[70:73]
	v_mfma_f32_16x16x32_bf16 v[66:69], v[186:189], v[218:221], v[66:69]
	v_mfma_f32_16x16x32_bf16 v[118:121], v[182:185], v[198:201], v[118:121]
	v_mfma_f32_16x16x32_bf16 v[114:117], v[190:193], v[198:201], v[114:117]
	v_mfma_f32_16x16x32_bf16 v[102:105], v[182:185], v[206:209], v[102:105]
	v_mfma_f32_16x16x32_bf16 v[98:101], v[190:193], v[206:209], v[98:101]
	v_mfma_f32_16x16x32_bf16 v[86:89], v[182:185], v[214:217], v[86:89]
	v_mfma_f32_16x16x32_bf16 v[82:85], v[190:193], v[214:217], v[82:85]
	v_mfma_f32_16x16x32_bf16 v[70:73], v[182:185], v[222:225], v[70:73]
	v_mfma_f32_16x16x32_bf16 v[66:69], v[190:193], v[222:225], v[66:69]
	s_setprio 0
	s_barrier
	s_add_i32 s54, s48, s38
	v_lshl_add_u64 v[170:171], s[28:29], 0, v[148:149]
	s_mov_b32 m0, s54
	ds_read_b128 v[194:197], v176 offset:16384
	ds_read_b128 v[198:201], v176 offset:17408
	ds_read_b128 v[202:205], v176 offset:18432
	ds_read_b128 v[206:209], v176 offset:19456
	ds_read_b128 v[210:213], v176 offset:20480
	ds_read_b128 v[214:217], v176 offset:21504
	ds_read_b128 v[218:221], v176 offset:22528
	ds_read_b128 v[222:225], v176 offset:23552
	global_load_lds_dwordx4 v[170:171], off
	s_add_i32 m0, s54, 0x2000
	s_add_u32 s54, s28, 0x100000
	v_lshl_add_u64 v[226:227], s[28:29], 0, v[152:153]
	s_addc_u32 s55, s29, 0
	s_add_i32 s57, s49, s38
	global_load_lds_dwordx4 v[226:227], off
	v_lshl_add_u64 v[228:229], s[54:55], 0, v[148:149]
	s_mov_b32 m0, s57
	v_lshl_add_u64 v[230:231], s[30:31], 0, v[150:151]
	global_load_lds_dwordx4 v[228:229], off
	v_lshl_add_u64 v[228:229], s[54:55], 0, v[152:153]
	s_add_i32 m0, s57, 0x2000
	s_nop 0
	global_load_lds_dwordx4 v[228:229], off
	v_lshl_add_u64 v[228:229], s[30:31], 0, v[146:147]
	s_mov_b32 m0, s39
	s_nop 0
	global_load_lds_dwordx4 v[228:229], off
	s_mov_b32 m0, s40
	s_nop 0
	global_load_lds_dwordx4 v[230:231], off
	s_cmp_lg_u32 s56, 0
	s_cbranch_scc1 .Lpg8r1
	s_waitcnt vmcnt(8)
	s_branch .Lpg8e1

.Lpg8e1:
	s_waitcnt lgkmcnt(0)
	s_barrier
	s_setprio 1
	s_waitcnt lgkmcnt(0)
	v_mfma_f32_16x16x32_bf16 v[62:65], v[134:137], v[194:197], v[62:65]
	v_mfma_f32_16x16x32_bf16 v[58:61], v[142:145], v[194:197], v[58:61]
	v_mfma_f32_16x16x32_bf16 v[46:49], v[134:137], v[202:205], v[46:49]
	v_mfma_f32_16x16x32_bf16 v[42:45], v[142:145], v[202:205], v[42:45]
	v_mfma_f32_16x16x32_bf16 v[30:33], v[134:137], v[210:213], v[30:33]
	v_mfma_f32_16x16x32_bf16 v[26:29], v[142:145], v[210:213], v[26:29]
	v_mfma_f32_16x16x32_bf16 v[14:17], v[134:137], v[218:221], v[14:17]
	v_mfma_f32_16x16x32_bf16 v[10:13], v[142:145], v[218:221], v[10:13]
	v_mfma_f32_16x16x32_bf16 v[62:65], v[138:141], v[198:201], v[62:65]
	v_mfma_f32_16x16x32_bf16 v[58:61], v[166:169], v[198:201], v[58:61]
	v_mfma_f32_16x16x32_bf16 v[46:49], v[138:141], v[206:209], v[46:49]
	v_mfma_f32_16x16x32_bf16 v[42:45], v[166:169], v[206:209], v[42:45]
	v_mfma_f32_16x16x32_bf16 v[30:33], v[138:141], v[214:217], v[30:33]
	v_mfma_f32_16x16x32_bf16 v[26:29], v[166:169], v[214:217], v[26:29]
	v_mfma_f32_16x16x32_bf16 v[14:17], v[138:141], v[222:225], v[14:17]
	v_mfma_f32_16x16x32_bf16 v[10:13], v[166:169], v[222:225], v[10:13]
	s_setprio 0
	s_setprio 1
	v_mfma_f32_16x16x32_bf16 v[54:57], v[178:181], v[194:197], v[54:57]
	v_mfma_f32_16x16x32_bf16 v[50:53], v[186:189], v[194:197], v[50:53]
	v_mfma_f32_16x16x32_bf16 v[38:41], v[178:181], v[202:205], v[38:41]
	v_mfma_f32_16x16x32_bf16 v[34:37], v[186:189], v[202:205], v[34:37]
	v_mfma_f32_16x16x32_bf16 v[22:25], v[178:181], v[210:213], v[22:25]
	v_mfma_f32_16x16x32_bf16 v[18:21], v[186:189], v[210:213], v[18:21]
	v_mfma_f32_16x16x32_bf16 v[6:9], v[178:181], v[218:221], v[6:9]
	v_mfma_f32_16x16x32_bf16 v[2:5], v[186:189], v[218:221], v[2:5]
	v_mfma_f32_16x16x32_bf16 v[54:57], v[182:185], v[198:201], v[54:57]
	v_mfma_f32_16x16x32_bf16 v[50:53], v[190:193], v[198:201], v[50:53]
	v_mfma_f32_16x16x32_bf16 v[38:41], v[182:185], v[206:209], v[38:41]
	v_mfma_f32_16x16x32_bf16 v[34:37], v[190:193], v[206:209], v[34:37]
	v_mfma_f32_16x16x32_bf16 v[22:25], v[182:185], v[214:217], v[22:25]
	v_mfma_f32_16x16x32_bf16 v[18:21], v[190:193], v[214:217], v[18:21]
	v_mfma_f32_16x16x32_bf16 v[6:9], v[182:185], v[222:225], v[6:9]
	v_mfma_f32_16x16x32_bf16 v[2:5], v[190:193], v[222:225], v[2:5]
	s_setprio 0
	s_barrier
	s_add_i32 s54, 0, 0x18000
	s_add_i32 s55, 0, 0x1c000
	v_add_u32_e32 v166, s54, v172
	v_add_u32_e32 v190, s55, v172
	ds_read_b128 v[134:137], v166
	ds_read_b128 v[138:141], v166 offset:1024
	ds_read_b128 v[142:145], v166 offset:2048
	ds_read_b128 v[166:169], v166 offset:3072
	ds_read_b128 v[178:181], v190
	ds_read_b128 v[182:185], v190 offset:1024
	ds_read_b128 v[186:189], v190 offset:2048
	ds_read_b128 v[190:193], v190 offset:3072
	s_add_u32 s30, s30, 0x100000
	s_addc_u32 s31, s31, 0
	s_mov_b32 m0, s41
	v_lshl_add_u64 v[232:233], s[30:31], 0, v[146:147]
	ds_read_b128 v[194:197], v176 offset:32768
	ds_read_b128 v[198:201], v176 offset:33792
	ds_read_b128 v[202:205], v176 offset:34816
	ds_read_b128 v[206:209], v176 offset:35840
	ds_read_b128 v[210:213], v176 offset:36864
	ds_read_b128 v[214:217], v176 offset:37888
	ds_read_b128 v[218:221], v176 offset:38912
	ds_read_b128 v[222:225], v176 offset:39936
	global_load_lds_dwordx4 v[232:233], off
	v_lshl_add_u64 v[232:233], s[30:31], 0, v[150:151]
	s_mov_b32 m0, s42
	s_nop 0
	global_load_lds_dwordx4 v[232:233], off
	s_waitcnt vmcnt(8)
	s_waitcnt lgkmcnt(0)
	s_barrier
	s_setprio 1
	s_waitcnt lgkmcnt(0)
	v_mfma_f32_16x16x32_bf16 v[126:129], v[134:137], v[194:197], v[126:129]
	v_mfma_f32_16x16x32_bf16 v[122:125], v[142:145], v[194:197], v[122:125]
	v_mfma_f32_16x16x32_bf16 v[110:113], v[134:137], v[202:205], v[110:113]
	v_mfma_f32_16x16x32_bf16 v[106:109], v[142:145], v[202:205], v[106:109]
	v_mfma_f32_16x16x32_bf16 v[94:97], v[134:137], v[210:213], v[94:97]
	v_mfma_f32_16x16x32_bf16 v[90:93], v[142:145], v[210:213], v[90:93]
	v_mfma_f32_16x16x32_bf16 v[78:81], v[134:137], v[218:221], v[78:81]
	v_mfma_f32_16x16x32_bf16 v[74:77], v[142:145], v[218:221], v[74:77]
	v_mfma_f32_16x16x32_bf16 v[126:129], v[138:141], v[198:201], v[126:129]
	v_mfma_f32_16x16x32_bf16 v[122:125], v[166:169], v[198:201], v[122:125]
	v_mfma_f32_16x16x32_bf16 v[110:113], v[138:141], v[206:209], v[110:113]
	v_mfma_f32_16x16x32_bf16 v[106:109], v[166:169], v[206:209], v[106:109]
	v_mfma_f32_16x16x32_bf16 v[94:97], v[138:141], v[214:217], v[94:97]
	v_mfma_f32_16x16x32_bf16 v[90:93], v[166:169], v[214:217], v[90:93]
	v_mfma_f32_16x16x32_bf16 v[78:81], v[138:141], v[222:225], v[78:81]
	v_mfma_f32_16x16x32_bf16 v[74:77], v[166:169], v[222:225], v[74:77]
	s_setprio 0
	s_setprio 1
	v_mfma_f32_16x16x32_bf16 v[118:121], v[178:181], v[194:197], v[118:121]
	v_mfma_f32_16x16x32_bf16 v[114:117], v[186:189], v[194:197], v[114:117]
	v_mfma_f32_16x16x32_bf16 v[102:105], v[178:181], v[202:205], v[102:105]
	v_mfma_f32_16x16x32_bf16 v[98:101], v[186:189], v[202:205], v[98:101]
	v_mfma_f32_16x16x32_bf16 v[86:89], v[178:181], v[210:213], v[86:89]
	v_mfma_f32_16x16x32_bf16 v[82:85], v[186:189], v[210:213], v[82:85]
	v_mfma_f32_16x16x32_bf16 v[70:73], v[178:181], v[218:221], v[70:73]
	v_mfma_f32_16x16x32_bf16 v[66:69], v[186:189], v[218:221], v[66:69]
	v_mfma_f32_16x16x32_bf16 v[118:121], v[182:185], v[198:201], v[118:121]
	v_mfma_f32_16x16x32_bf16 v[114:117], v[190:193], v[198:201], v[114:117]
	v_mfma_f32_16x16x32_bf16 v[102:105], v[182:185], v[206:209], v[102:105]
	v_mfma_f32_16x16x32_bf16 v[98:101], v[190:193], v[206:209], v[98:101]
	v_mfma_f32_16x16x32_bf16 v[86:89], v[182:185], v[214:217], v[86:89]
	v_mfma_f32_16x16x32_bf16 v[82:85], v[190:193], v[214:217], v[82:85]
	v_mfma_f32_16x16x32_bf16 v[70:73], v[182:185], v[222:225], v[70:73]
	v_mfma_f32_16x16x32_bf16 v[66:69], v[190:193], v[222:225], v[66:69]
	s_setprio 0
	s_barrier
	s_add_i32 s30, s54, s38
	v_lshl_add_u64 v[170:171], v[170:171], 0, s[10:11]
	s_mov_b32 m0, s30
	ds_read_b128 v[194:197], v176 offset:49152
	ds_read_b128 v[198:201], v176 offset:50176
	ds_read_b128 v[202:205], v176 offset:51200
	ds_read_b128 v[206:209], v176 offset:52224
	ds_read_b128 v[210:213], v176 offset:53248
	ds_read_b128 v[214:217], v176 offset:54272
	ds_read_b128 v[218:221], v176 offset:55296
	ds_read_b128 v[222:225], v176 offset:56320
	global_load_lds_dwordx4 v[170:171], off
	s_add_i32 m0, s30, 0x2000
	s_add_u32 s28, s28, 0x100080
	v_lshl_add_u64 v[170:171], v[226:227], 0, s[10:11]
	s_addc_u32 s29, s29, 0
	s_add_i32 s30, s55, s38
	global_load_lds_dwordx4 v[170:171], off
	v_lshl_add_u64 v[170:171], s[28:29], 0, v[148:149]
	s_mov_b32 m0, s30
	s_nop 0
	global_load_lds_dwordx4 v[170:171], off
	v_lshl_add_u64 v[170:171], s[28:29], 0, v[152:153]
	s_add_i32 m0, s30, 0x2000
	s_nop 0
	global_load_lds_dwordx4 v[170:171], off
	v_lshl_add_u64 v[170:171], v[228:229], 0, s[10:11]
	s_mov_b32 m0, s33
	s_nop 0
	global_load_lds_dwordx4 v[170:171], off
	v_lshl_add_u64 v[170:171], v[230:231], 0, s[10:11]
	s_mov_b32 m0, s44
	s_nop 0
	global_load_lds_dwordx4 v[170:171], off
	s_waitcnt vmcnt(8)
	s_waitcnt lgkmcnt(0)
	s_barrier
	s_setprio 1
	s_waitcnt lgkmcnt(0)
	v_mfma_f32_16x16x32_bf16 v[62:65], v[134:137], v[194:197], v[62:65]
	v_mfma_f32_16x16x32_bf16 v[58:61], v[142:145], v[194:197], v[58:61]
	v_mfma_f32_16x16x32_bf16 v[46:49], v[134:137], v[202:205], v[46:49]
	v_mfma_f32_16x16x32_bf16 v[42:45], v[142:145], v[202:205], v[42:45]
	v_mfma_f32_16x16x32_bf16 v[30:33], v[134:137], v[210:213], v[30:33]
	v_mfma_f32_16x16x32_bf16 v[26:29], v[142:145], v[210:213], v[26:29]
	v_mfma_f32_16x16x32_bf16 v[14:17], v[134:137], v[218:221], v[14:17]
	v_mfma_f32_16x16x32_bf16 v[10:13], v[142:145], v[218:221], v[10:13]
	v_mfma_f32_16x16x32_bf16 v[62:65], v[138:141], v[198:201], v[62:65]
	v_mfma_f32_16x16x32_bf16 v[58:61], v[166:169], v[198:201], v[58:61]
	v_mfma_f32_16x16x32_bf16 v[46:49], v[138:141], v[206:209], v[46:49]
	v_mfma_f32_16x16x32_bf16 v[42:45], v[166:169], v[206:209], v[42:45]
	v_mfma_f32_16x16x32_bf16 v[30:33], v[138:141], v[214:217], v[30:33]
	v_mfma_f32_16x16x32_bf16 v[26:29], v[166:169], v[214:217], v[26:29]
	v_mfma_f32_16x16x32_bf16 v[14:17], v[138:141], v[222:225], v[14:17]
	v_mfma_f32_16x16x32_bf16 v[10:13], v[166:169], v[222:225], v[10:13]
	s_setprio 0
	s_setprio 1
	v_mfma_f32_16x16x32_bf16 v[54:57], v[178:181], v[194:197], v[54:57]
	v_mfma_f32_16x16x32_bf16 v[50:53], v[186:189], v[194:197], v[50:53]
	v_mfma_f32_16x16x32_bf16 v[38:41], v[178:181], v[202:205], v[38:41]
	v_mfma_f32_16x16x32_bf16 v[34:37], v[186:189], v[202:205], v[34:37]
	v_mfma_f32_16x16x32_bf16 v[22:25], v[178:181], v[210:213], v[22:25]
	v_mfma_f32_16x16x32_bf16 v[18:21], v[186:189], v[210:213], v[18:21]
	v_mfma_f32_16x16x32_bf16 v[6:9], v[178:181], v[218:221], v[6:9]
	v_mfma_f32_16x16x32_bf16 v[2:5], v[186:189], v[218:221], v[2:5]
	v_mfma_f32_16x16x32_bf16 v[54:57], v[182:185], v[198:201], v[54:57]
	v_mfma_f32_16x16x32_bf16 v[50:53], v[190:193], v[198:201], v[50:53]
	v_mfma_f32_16x16x32_bf16 v[38:41], v[182:185], v[206:209], v[38:41]
	v_mfma_f32_16x16x32_bf16 v[34:37], v[190:193], v[206:209], v[34:37]
	v_mfma_f32_16x16x32_bf16 v[22:25], v[182:185], v[214:217], v[22:25]
	v_mfma_f32_16x16x32_bf16 v[18:21], v[190:193], v[214:217], v[18:21]
	v_mfma_f32_16x16x32_bf16 v[6:9], v[182:185], v[222:225], v[6:9]
	v_mfma_f32_16x16x32_bf16 v[2:5], v[190:193], v[222:225], v[2:5]
	s_setprio 0
	s_barrier
	s_add_i32 s53, s53, 2
	s_add_u32 s26, s26, 0x100
	s_addc_u32 s27, s27, 0
	s_cmp_gt_u32 s53, 61
	s_cbranch_scc0 .LBB0_111
	s_and_b64 vcc, exec, s[12:13]
	s_cbranch_vccz .LBB0_114
	s_barrier

.LBB0_251:
	v_lshlrev_b32_e32 v3, 4, v74
	s_lshl_b32 s12, s33, 10
	s_add_i32 s12, s12, 0x18400
	v_add_u32_e32 v3, s12, v3
	ds_read_b128 v[104:107], v3
	ds_read_b128 v[108:111], v3 offset:8192
	ds_read_b128 v[112:115], v3 offset:16384
	s_waitcnt lgkmcnt(0)
	s_add_i32 s77, s77, 1
	s_mov_b64 s[12:13], 0

.LBB0_258:
	s_bfe_u32 s17, s16, 0x30003
	v_cvt_f32_ubyte0_e32 v3, s17
	v_sub_f32_e32 v3, 0xc0a00000, v3
	v_cmp_gt_f32_e32 vcc, s63, v3
	s_and_b64 s[12:13], vcc, exec
	s_cselect_b32 s12, 0xffffffc0, 0
	v_cndmask_b32_e32 v4, 0, v150, vcc
	v_add_f32_e32 v3, v3, v4
	v_exp_f32_e32 v3, v3
	s_mov_b32 s20, s21
	s_mov_b32 s22, s21
	s_mov_b32 s23, s21
	v_ldexp_f32 v3, v3, s12
	v_sub_f32_e32 v3, 1.0, v3
	v_cmp_gt_f32_e32 vcc, s64, v3
	s_and_b64 s[12:13], vcc, exec
	s_cselect_b32 s12, 32, 0
	v_ldexp_f32 v3, v3, s12
	v_log_f32_e32 v3, v3
	v_cndmask_b32_e32 v4, 0, v151, vcc
	s_barrier
	v_sub_f32_e32 v3, v3, v4
	v_mul_f32_e32 v4, v3, v103
	v_cmp_gt_f32_e32 vcc, s63, v4
	v_mul_f32_e32 v5, v3, v104
	s_and_b64 s[12:13], vcc, exec
	v_cndmask_b32_e32 v4, 0, v150, vcc
	v_fmac_f32_e32 v4, v3, v103
	v_cmp_gt_f32_e32 vcc, s63, v5
	v_exp_f32_e32 v4, v4
	s_cselect_b32 s12, 0xffffffc0, 0
	v_cndmask_b32_e32 v5, 0, v150, vcc
	v_fmac_f32_e32 v5, v3, v104
	v_exp_f32_e32 v5, v5
	v_ldexp_f32 v160, v4, s12
	s_and_b64 s[12:13], vcc, exec
	v_mul_f32_e32 v4, v3, v105
	s_cselect_b32 s12, 0xffffffc0, 0
	v_cmp_gt_f32_e32 vcc, s63, v4
	v_ldexp_f32 v161, v5, s12
	v_mul_f32_e32 v5, v3, v106
	v_cndmask_b32_e32 v4, 0, v150, vcc
	v_fmac_f32_e32 v4, v3, v105
	s_and_b64 s[12:13], vcc, exec
	v_cmp_gt_f32_e32 vcc, s63, v5
	v_exp_f32_e32 v4, v4
	s_cselect_b32 s12, 0xffffffc0, 0
	v_cndmask_b32_e32 v5, 0, v150, vcc
	v_fmac_f32_e32 v5, v3, v106
	v_exp_f32_e32 v5, v5
	v_ldexp_f32 v162, v4, s12
	s_and_b64 s[12:13], vcc, exec
	v_mul_f32_e32 v4, v3, v107
	s_cselect_b32 s12, 0xffffffc0, 0
	v_cmp_gt_f32_e32 vcc, s63, v4
	v_ldexp_f32 v163, v5, s12
	v_mul_f32_e32 v5, v3, v108
	v_cndmask_b32_e32 v4, 0, v150, vcc
	v_fmac_f32_e32 v4, v3, v107
	s_and_b64 s[12:13], vcc, exec
	v_cmp_gt_f32_e32 vcc, s63, v5
	v_exp_f32_e32 v4, v4
	s_cselect_b32 s12, 0xffffffc0, 0
	v_cndmask_b32_e32 v5, 0, v150, vcc
	v_fmac_f32_e32 v5, v3, v108
	v_exp_f32_e32 v5, v5
	v_ldexp_f32 v164, v4, s12
	s_and_b64 s[12:13], vcc, exec
	v_mul_f32_e32 v4, v3, v109
	s_cselect_b32 s12, 0xffffffc0, 0
	v_cmp_gt_f32_e32 vcc, s63, v4
	v_ldexp_f32 v165, v5, s12
	v_mul_f32_e32 v5, v3, v110
	v_cndmask_b32_e32 v4, 0, v150, vcc
	v_fmac_f32_e32 v4, v3, v109
	s_and_b64 s[12:13], vcc, exec
	v_cmp_gt_f32_e32 vcc, s63, v5
	v_exp_f32_e32 v4, v4
	s_cselect_b32 s12, 0xffffffc0, 0
	v_cndmask_b32_e32 v5, 0, v150, vcc
	v_fmac_f32_e32 v5, v3, v110
	v_exp_f32_e32 v5, v5
	v_ldexp_f32 v166, v4, s12
	s_and_b64 s[12:13], vcc, exec
	s_cselect_b32 s12, 0xffffffc0, 0
	v_mul_f32_e32 v4, v3, v111
	v_ldexp_f32 v167, v5, s12
	v_cmp_gt_f32_e32 vcc, s63, v4
	v_mul_f32_e32 v5, v3, v112
	v_cmp_gt_f32_e64 s[12:13], s63, v5
	v_cndmask_b32_e32 v4, 0, v150, vcc
	v_fmac_f32_e32 v4, v3, v111
	v_cndmask_b32_e64 v5, 0, v150, s[12:13]
	v_exp_f32_e32 v4, v4
	v_fmac_f32_e32 v5, v3, v112
	v_exp_f32_e32 v5, v5
	v_cndmask_b32_e32 v6, 0, v152, vcc
	v_ldexp_f32 v168, v4, v6
	v_cndmask_b32_e64 v4, 0, v152, s[12:13]
	v_ldexp_f32 v169, v5, v4
	v_mul_f32_e32 v4, v3, v113
	v_cmp_gt_f32_e32 vcc, s63, v4
	v_mul_f32_e32 v5, v3, v114
	v_cmp_gt_f32_e64 s[12:13], s63, v5
	v_cndmask_b32_e32 v4, 0, v150, vcc
	v_fmac_f32_e32 v4, v3, v113
	v_cndmask_b32_e64 v5, 0, v150, s[12:13]
	v_exp_f32_e32 v4, v4
	v_fmac_f32_e32 v5, v3, v114
	v_exp_f32_e32 v5, v5
	v_cndmask_b32_e32 v6, 0, v152, vcc
	v_ldexp_f32 v170, v4, v6
	v_cndmask_b32_e64 v4, 0, v152, s[12:13]
	v_ldexp_f32 v171, v5, v4
	v_mul_f32_e32 v4, v3, v1
	v_mul_f32_e32 v5, 0x43000000, v3
	v_cmp_gt_f32_e32 vcc, s63, v4
	s_ashr_i32 s14, s16, 6
	v_mul_f32_e32 v6, v3, v75
	v_cndmask_b32_e32 v4, 0, v150, vcc
	v_cndmask_b32_e32 v8, 0, v152, vcc
	v_cmp_gt_f32_e32 vcc, s63, v5
	v_fmac_f32_e32 v4, v3, v1
	v_exp_f32_e32 v4, v4
	v_cndmask_b32_e32 v5, 0, v150, vcc
	v_fmac_f32_e32 v5, 0x43000000, v3
	v_exp_f32_e32 v5, v5
	s_and_b64 s[12:13], vcc, exec
	v_mul_f32_e32 v7, v3, v100
	s_cselect_b32 s12, 0xffffffc0, 0
	v_cmp_gt_f32_e32 vcc, s63, v6
	v_ldexp_f32 v86, v4, v8
	v_ldexp_f32 v88, v5, s12
	v_cndmask_b32_e32 v4, 0, v150, vcc
	v_cmp_gt_f32_e64 s[12:13], s63, v7
	v_fmac_f32_e32 v4, v3, v75
	v_exp_f32_e32 v4, v4
	v_cndmask_b32_e64 v5, 0, v150, s[12:13]
	v_fmac_f32_e32 v5, v3, v100
	v_exp_f32_e32 v3, v5
	v_cndmask_b32_e32 v5, 0, v152, vcc
	v_ldexp_f32 v172, v4, v5
	v_cndmask_b32_e64 v4, 0, v152, s[12:13]
	v_ldexp_f32 v173, v3, v4
	v_mov_b64_e32 v[4:5], s[20:21]
	s_ashr_i32 s15, s14, 31
	v_mov_b64_e32 v[6:7], s[22:23]
	s_lshl_b64 s[12:13], s[14:15], 11
	ds_write_b128 v115, v[4:7]
	ds_write_b128 v115, v[4:7] offset:16
	v_lshl_add_u64 v[4:5], v[76:77], 0, s[12:13]
	s_lshl_b32 s12, s16, 6
	v_lshlrev_b64 v[6:7], 12, v[4:5]
	s_and_b32 s12, s12, 0x1c0
	s_mul_i32 s15, s14, 0x3000000
	v_or_b32_e32 v6, s12, v6
	s_mul_hi_i32 s13, s14, 0x3000000
	s_or_b32 s12, s15, s12
	v_lshl_add_u64 v[94:95], v[80:81], 0, s[12:13]
	v_mad_u64_u32 v[98:99], s[12:13], v4, s62, v[84:85]
	v_mov_b32_e32 v4, v99
	v_mad_u64_u32 v[4:5], s[12:13], v5, s62, v[4:5]
	v_mov_b32_e32 v18, 0
	v_mov_b32_e32 v90, v88
	v_mov_b32_e32 v91, v88
	v_mov_b32_e32 v87, v86
	s_lshl_b32 s20, s17, 9
	v_lshl_add_u64 v[92:93], v[78:79], 0, v[6:7]
	v_mad_i64_i32 v[96:97], s[12:13], s14, v153, v[82:83]
	v_mov_b32_e32 v99, v4
	s_mov_b32 s22, 16
	v_mov_b32_e32 v19, v18
	v_mov_b32_e32 v20, v18
	v_mov_b32_e32 v21, v18
	v_mov_b32_e32 v10, v18
	v_mov_b32_e32 v11, v18
	v_mov_b32_e32 v12, v18
	v_mov_b32_e32 v13, v18
	v_mov_b32_e32 v14, v18
	v_mov_b32_e32 v15, v18
	v_mov_b32_e32 v16, v18
	v_mov_b32_e32 v17, v18
	v_mov_b32_e32 v6, v18
	v_mov_b32_e32 v7, v18
	v_mov_b32_e32 v8, v18
	v_mov_b32_e32 v9, v18
	v_lshlrev_b32_e32 v3, 4, v74
	s_lshl_b32 s12, s33, 10
	s_add_i32 s12, s12, 0x18400
	v_add_u32_e32 v3, s12, v3
	ds_write_b128 v3, v[104:107]
	ds_write_b128 v3, v[108:111] offset:8192
	ds_write_b128 v3, v[112:115] offset:16384
	v_lshl_add_u64 v[54:55], v[96:97], 0, s[20:21]
	v_add_co_u32_e32 v56, vcc, s65, v54
	s_nop 1
	v_addc_co_u32_e32 v57, vcc, 0, v55, vcc
	v_add_co_u32_e32 v58, vcc, s66, v54
	s_nop 1
	v_addc_co_u32_e32 v59, vcc, 0, v55, vcc
	global_load_dwordx4 v[196:199], v[56:57], off
	global_load_dwordx4 v[200:203], v[58:59], off
	v_add_co_u32_e32 v56, vcc, s67, v54
	s_nop 1
	v_addc_co_u32_e32 v57, vcc, 0, v55, vcc
	v_add_co_u32_e32 v58, vcc, s68, v54
	s_nop 1
	v_addc_co_u32_e32 v59, vcc, 0, v55, vcc
	global_load_dwordx4 v[204:207], v[56:57], off
	global_load_dwordx4 v[208:211], v[58:59], off
	v_add_co_u32_e32 v56, vcc, s69, v54
	s_nop 1
	v_addc_co_u32_e32 v57, vcc, 0, v55, vcc
	v_add_co_u32_e32 v58, vcc, s70, v54
	s_nop 1
	v_addc_co_u32_e32 v59, vcc, 0, v55, vcc
	global_load_dwordx4 v[212:215], v[56:57], off
	global_load_dwordx4 v[216:219], v[58:59], off
	v_add_co_u32_e32 v56, vcc, s71, v54
	s_nop 1
	v_addc_co_u32_e32 v57, vcc, 0, v55, vcc
	v_add_co_u32_e32 v58, vcc, s72, v54
	s_nop 1
	v_addc_co_u32_e32 v59, vcc, 0, v55, vcc
	global_load_dwordx4 v[220:223], v[56:57], off
	global_load_dwordx4 v[224:227], v[58:59], off
	v_lshl_add_u64 v[54:55], v[94:95], 0, s[20:21]
	v_add_co_u32_e32 v56, vcc, s73, v54
	s_nop 1
	v_addc_co_u32_e32 v57, vcc, 0, v55, vcc
	global_load_dwordx2 v[228:229], v[56:57], off
	v_add_co_u32_e32 v58, vcc, s75, v54
	s_nop 1
	v_addc_co_u32_e32 v59, vcc, 0, v55, vcc
	global_load_dwordx2 v[230:231], v[58:59], off
	v_lshl_add_u64 v[54:55], v[98:99], 0, s[20:21]
	global_load_dwordx4 v[232:235], v[54:55], off offset:-256
	global_load_dwordx4 v[236:239], v[54:55], off offset:-192
	global_load_dwordx4 v[240:243], v[54:55], off offset:-128
	global_load_dwordx4 v[244:247], v[54:55], off offset:-64
	global_load_dwordx4 v[248:251], v[54:55], off
	global_load_dwordx4 v[104:107], v[54:55], off offset:64
	global_load_dwordx4 v[108:111], v[54:55], off offset:128
	global_load_dwordx4 v[112:115], v[54:55], off offset:192
	s_branch .LBB0_260
.LBB0_259:
	ds_read_b128 v[58:61], v117
	ds_read_b128 v[62:65], v117 offset:8192
	ds_read_b128 v[66:69], v118
	s_nop 0
	v_mov_b32_e32 v4, v70
	v_mov_b32_e32 v5, v72
	s_waitcnt lgkmcnt(2)
	v_mfma_f32_16x16x32_bf16 v[58:61], v[58:61], v[50:53], 0
	v_mov_b32_e32 v72, v71
	v_mov_b32_e32 v89, v88
	v_pk_mul_f32 v[20:21], v[88:89], v[20:21]
	s_waitcnt lgkmcnt(1)
	v_mfma_f32_16x16x32_bf16 v[50:53], v[62:65], v[50:53], 0
	ds_read_b128 v[62:65], v118 offset:8192
	v_pk_mul_f32 v[18:19], v[90:91], v[18:19]
	v_pk_mul_f32 v[16:17], v[88:89], v[16:17]
	s_waitcnt lgkmcnt(1)
	v_mfma_f32_16x16x32_bf16 v[58:61], v[66:69], v[46:49], v[58:61]
	ds_read_b128 v[66:69], v119
	v_pk_mul_f32 v[14:15], v[90:91], v[14:15]
	v_lshl_add_u64 v[194:195], v[92:93], 0, s[20:21]
	s_waitcnt lgkmcnt(1)
	v_mfma_f32_16x16x32_bf16 v[46:49], v[62:65], v[46:49], v[50:53]
	s_nop 2
	ds_read_b128 v[50:53], v120
	ds_read_b128 v[62:65], v119 offset:8192
	v_pk_mul_f32 v[8:9], v[88:89], v[8:9]
	v_pk_mul_f32 v[6:7], v[90:91], v[6:7]
	s_waitcnt lgkmcnt(2)
	v_mfma_f32_16x16x32_bf16 v[58:61], v[66:69], v[42:45], v[58:61]
	ds_read_b128 v[66:69], v121
	ds_read_b128 v[174:177], v120 offset:8192
	v_pk_mul_f32 v[12:13], v[88:89], v[12:13]
	v_pk_mul_f32 v[10:11], v[90:91], v[10:11]
	s_waitcnt lgkmcnt(3)
	v_mfma_f32_16x16x32_bf16 v[50:53], v[50:53], v[38:41], v[58:61]
	s_nop 2
	ds_read_b128 v[58:61], v122
	ds_read_b128 v[178:181], v121 offset:8192
	s_add_i32 s22, s22, -1
	v_lshl_add_u64 v[92:93], v[92:93], 0, s[56:57]
	s_waitcnt lgkmcnt(4)
	v_mfma_f32_16x16x32_bf16 v[42:45], v[62:65], v[42:45], v[46:49]
	v_lshl_add_u64 v[94:95], v[94:95], 0, s[58:59]
	v_lshl_add_u64 v[96:97], v[96:97], 0, s[58:59]
	s_cmp_eq_u32 s22, 0
	s_waitcnt lgkmcnt(3)
	v_mfma_f32_16x16x32_bf16 v[50:53], v[66:69], v[34:37], v[50:53]
	ds_read_b128 v[66:69], v123
	ds_read_b128 v[182:185], v122 offset:8192
	ds_read_b128 v[186:189], v124
	v_lshl_add_u64 v[98:99], v[98:99], 0, s[58:59]
	s_waitcnt lgkmcnt(5)
	v_mfma_f32_16x16x32_bf16 v[38:41], v[174:177], v[38:41], v[42:45]
	s_waitcnt lgkmcnt(4)
	v_mfma_f32_16x16x32_bf16 v[50:53], v[58:61], v[30:33], v[50:53]
	ds_read_b128 v[58:61], v123 offset:8192
	ds_read_b128 v[190:193], v124 offset:8192
	s_waitcnt lgkmcnt(5)
	v_mfma_f32_16x16x32_bf16 v[34:37], v[178:181], v[34:37], v[38:41]
	s_waitcnt lgkmcnt(4)
	v_mfma_f32_16x16x32_bf16 v[50:53], v[66:69], v[26:29], v[50:53]
	s_waitcnt lgkmcnt(3)
	v_mfma_f32_16x16x32_bf16 v[30:33], v[182:185], v[30:33], v[34:37]
	s_nop 3
	ds_read_b128 v[34:37], v125
	s_waitcnt lgkmcnt(3)
	v_mfma_f32_16x16x32_bf16 v[50:53], v[186:189], v[22:25], v[50:53]
	s_waitcnt lgkmcnt(2)
	v_mfma_f32_16x16x32_bf16 v[26:29], v[58:61], v[26:29], v[30:33]
	s_nop 2
	ds_read_b128 v[30:33], v125 offset:4352
	ds_read_b64_tr_b16 v[38:39], v126
	ds_read_b64_tr_b16 v[40:41], v127 offset:1024
	v_mov_b32_e32 v66, v50
	v_mov_b32_e32 v67, v52
	v_mov_b32_e32 v52, v51
	v_pk_fma_f32 v[4:5], v[86:87], v[66:67], v[4:5]
	v_pk_fma_f32 v[50:51], v[86:87], v[52:53], v[72:73]
	v_and_b32_sdwa v46, v4, v159 dst_sel:DWORD dst_unused:UNUSED_PAD src0_sel:WORD_1 src1_sel:DWORD
	v_and_b32_sdwa v47, v51, v159 dst_sel:DWORD dst_unused:UNUSED_PAD src0_sel:WORD_1 src1_sel:DWORD
	v_and_b32_sdwa v48, v50, v159 dst_sel:DWORD dst_unused:UNUSED_PAD src0_sel:WORD_1 src1_sel:DWORD
	v_add3_u32 v62, v4, v46, s74
	v_add3_u32 v4, v51, v47, s74
	v_add3_u32 v63, v50, v48, s74
	s_waitcnt lgkmcnt(4)
	v_mfma_f32_16x16x32_bf16 v[22:25], v[190:193], v[22:25], v[26:29]
	s_nop 2
	ds_read_b128 v[26:29], v125 offset:64
	ds_read_b64_tr_b16 v[42:43], v127 offset:9216
	ds_read_b64_tr_b16 v[44:45], v127 offset:17408
	ds_read_b64_tr_b16 v[46:47], v128
	ds_read_b64_tr_b16 v[48:49], v129 offset:1024
	ds_read_b128 v[50:53], v125 offset:4416
	v_and_b32_sdwa v3, v5, v159 dst_sel:DWORD dst_unused:UNUSED_PAD src0_sel:WORD_1 src1_sel:DWORD
	s_waitcnt lgkmcnt(6)
	v_mfma_f32_16x16x32_bf16 v[18:21], v[34:37], v[38:41], v[18:21]
	v_add3_u32 v3, v5, v3, s74
	v_and_b32_e32 v64, 0xffff0000, v4
	v_mfma_f32_16x16x32_bf16 v[14:17], v[30:33], v[38:41], v[14:17]
	ds_read_b64_tr_b16 v[38:39], v129 offset:9216
	ds_read_b64_tr_b16 v[60:61], v127 offset:25600
	ds_read_b64_tr_b16 v[40:41], v130
	s_waitcnt lgkmcnt(4)
	v_mfma_f32_16x16x32_bf16 v[4:7], v[30:33], v[46:49], v[6:9]
	v_and_b32_e32 v32, 0xffff0000, v63
	v_or_b32_sdwa v33, v64, v3 dst_sel:DWORD dst_unused:UNUSED_PAD src0_sel:DWORD src1_sel:WORD_1
	v_or_b32_sdwa v32, v32, v62 dst_sel:DWORD dst_unused:UNUSED_PAD src0_sel:DWORD src1_sel:WORD_1
	s_waitcnt lgkmcnt(0)
	v_mfma_f32_16x16x32_bf16 v[18:21], v[26:29], v[40:43], v[18:21]
	v_mfma_f32_16x16x32_bf16 v[14:17], v[50:53], v[40:43], v[14:17]
	v_add_co_u32_e32 v40, vcc, s76, v194
	s_nop 1
	v_addc_co_u32_e32 v41, vcc, 0, v195, vcc
	v_mfma_f32_16x16x32_bf16 v[10:13], v[34:37], v[46:49], v[10:13]
	ds_read_b64_tr_b16 v[36:37], v131
	ds_read_b64_tr_b16 v[8:9], v129 offset:17408
	ds_read_b64_tr_b16 v[30:31], v129 offset:25600
	global_store_dwordx2 v[40:41], v[32:33], off
	ds_read_b128 v[32:35], v125 offset:128
	ds_read_b128 v[46:49], v125 offset:4480
	ds_read_b64_tr_b16 v[42:43], v132
	s_waitcnt lgkmcnt(5)
	v_mfma_f32_16x16x32_bf16 v[10:13], v[26:29], v[36:39], v[10:13]
	v_mov_b32_e32 v27, v24
	v_mov_b32_e32 v24, v23
	v_mov_b32_e32 v26, v22
	v_mfma_f32_16x16x32_bf16 v[36:39], v[50:53], v[36:39], v[4:7]
	ds_read_b128 v[50:53], v125 offset:192
	s_nop 1
	ds_read_b64_tr_b16 v[6:7], v133
	ds_read_b64_tr_b16 v[58:59], v134
	ds_read_b64_tr_b16 v[28:29], v135
	v_mov_b32_e32 v5, v56
	v_mov_b32_e32 v56, v55
	s_waitcnt lgkmcnt(4)
	v_mfma_f32_16x16x32_bf16 v[18:21], v[32:35], v[42:45], v[18:21]
	v_mov_b32_e32 v4, v54
	v_pk_fma_f32 v[22:23], v[86:87], v[24:25], v[56:57]
	v_pk_fma_f32 v[26:27], v[86:87], v[26:27], v[4:5]
	s_waitcnt lgkmcnt(1)
	v_mfma_f32_16x16x32_bf16 v[18:21], v[50:53], v[58:61], v[18:21]
	v_and_b32_sdwa v3, v27, v159 dst_sel:DWORD dst_unused:UNUSED_PAD src0_sel:WORD_1 src1_sel:DWORD
	v_and_b32_sdwa v24, v22, v159 dst_sel:DWORD dst_unused:UNUSED_PAD src0_sel:WORD_1 src1_sel:DWORD
	v_add3_u32 v3, v27, v3, s74
	v_mfma_f32_16x16x32_bf16 v[10:13], v[32:35], v[6:9], v[10:13]
	v_add3_u32 v22, v22, v24, s74
	v_and_b32_e32 v22, 0xffff0000, v22
	ds_read_b128 v[62:65], v125 offset:4544
	v_mfma_f32_16x16x32_bf16 v[4:7], v[46:49], v[6:9], v[36:39]
	v_and_b32_sdwa v9, v23, v159 dst_sel:DWORD dst_unused:UNUSED_PAD src0_sel:WORD_1 src1_sel:DWORD
	v_add3_u32 v9, v23, v9, s74
	v_and_b32_sdwa v8, v26, v159 dst_sel:DWORD dst_unused:UNUSED_PAD src0_sel:WORD_1 src1_sel:DWORD
	v_and_b32_e32 v9, 0xffff0000, v9
	v_add3_u32 v8, v26, v8, s74
	v_or_b32_sdwa v9, v9, v3 dst_sel:DWORD dst_unused:UNUSED_PAD src0_sel:DWORD src1_sel:WORD_1
	v_bfe_u32 v3, v18, 16, 1
	v_or_b32_sdwa v8, v22, v8 dst_sel:DWORD dst_unused:UNUSED_PAD src0_sel:DWORD src1_sel:WORD_1
	v_add3_u32 v3, v18, v3, s74
	global_store_dwordx2 v[40:41], v[8:9], off offset:32
	s_waitcnt lgkmcnt(0)
	s_barrier
	ds_write_b16_d16_hi v136, v3
	v_bfe_u32 v3, v19, 16, 1
	v_add3_u32 v3, v19, v3, s74
	v_mfma_f32_16x16x32_bf16 v[10:13], v[50:53], v[28:31], v[10:13]
	ds_write_b16_d16_hi v137, v3
	v_bfe_u32 v3, v20, 16, 1
	v_add3_u32 v3, v20, v3, s74
	ds_write_b16_d16_hi v138, v3
	v_bfe_u32 v3, v21, 16, 1
	v_add3_u32 v3, v21, v3, s74
	v_mfma_f32_16x16x32_bf16 v[14:17], v[46:49], v[42:45], v[14:17]
	ds_write_b16_d16_hi v139, v3
	v_bfe_u32 v3, v10, 16, 1
	v_add3_u32 v3, v10, v3, s74
	ds_write_b16_d16_hi v140, v3
	v_bfe_u32 v3, v11, 16, 1
	v_add3_u32 v3, v11, v3, s74
	v_mfma_f32_16x16x32_bf16 v[14:17], v[62:65], v[58:61], v[14:17]
	ds_write_b16_d16_hi v141, v3
	v_bfe_u32 v3, v12, 16, 1
	v_add3_u32 v3, v12, v3, s74
	ds_write_b16_d16_hi v142, v3
	v_bfe_u32 v3, v13, 16, 1
	v_add3_u32 v3, v13, v3, s74
	ds_write_b16_d16_hi v143, v3
	s_nop 0
	v_bfe_u32 v3, v14, 16, 1
	v_add3_u32 v3, v14, v3, s74
	ds_write_b16_d16_hi v136, v3 offset:8192
	v_bfe_u32 v3, v15, 16, 1
	v_add3_u32 v3, v15, v3, s74
	v_mfma_f32_16x16x32_bf16 v[6:9], v[62:65], v[28:31], v[4:7]
	ds_write_b16_d16_hi v144, v3 offset:8704
	v_bfe_u32 v3, v16, 16, 1
	v_add3_u32 v3, v16, v3, s74
	ds_write_b16_d16_hi v145, v3 offset:9216
	v_bfe_u32 v3, v17, 16, 1
	v_add3_u32 v3, v17, v3, s74
	ds_write_b16_d16_hi v146, v3 offset:9728
	s_nop 0
	v_bfe_u32 v3, v6, 16, 1
	v_add3_u32 v3, v6, v3, s74
	ds_write_b16_d16_hi v140, v3 offset:8192
	v_bfe_u32 v3, v7, 16, 1
	v_add3_u32 v3, v7, v3, s74
	ds_write_b16_d16_hi v147, v3 offset:8704
	v_bfe_u32 v3, v8, 16, 1
	v_add3_u32 v3, v8, v3, s74
	ds_write_b16_d16_hi v148, v3 offset:9216
	v_bfe_u32 v3, v9, 16, 1
	v_add3_u32 v3, v9, v3, s74
	ds_write_b16_d16_hi v149, v3 offset:9728
	s_cbranch_scc1 .LBB0_251
.LBB0_260:
	s_waitcnt vmcnt(0)
	ds_write_b128 v116, v[196:199]
	ds_write_b128 v116, v[200:203] offset:4096
	ds_write_b128 v116, v[204:207] offset:8192
	ds_write_b128 v116, v[208:211] offset:12288
	ds_write_b128 v116, v[212:215] offset:16384
	ds_write_b128 v116, v[216:219] offset:20480
	ds_write_b128 v116, v[220:223] offset:24576
	ds_write_b128 v116, v[224:227] offset:28672
	v_mov_b32_e32 v186, v228
	v_mov_b32_e32 v187, v229
	v_mov_b32_e32 v4, v230
	v_mov_b32_e32 v5, v231
	v_mov_b64_e32 v[50:51], v[232:233]
	v_mov_b64_e32 v[52:53], v[234:235]
	v_mov_b64_e32 v[46:47], v[236:237]
	v_mov_b64_e32 v[48:49], v[238:239]
	v_mov_b64_e32 v[42:43], v[240:241]
	v_mov_b64_e32 v[44:45], v[242:243]
	v_mov_b64_e32 v[38:39], v[244:245]
	v_mov_b64_e32 v[40:41], v[246:247]
	v_mov_b64_e32 v[34:35], v[248:249]
	v_mov_b64_e32 v[36:37], v[250:251]
	v_mov_b64_e32 v[30:31], v[104:105]
	v_mov_b64_e32 v[32:33], v[106:107]
	v_mov_b64_e32 v[26:27], v[108:109]
	v_mov_b64_e32 v[28:29], v[110:111]
	v_mov_b64_e32 v[22:23], v[112:113]
	v_mov_b64_e32 v[24:25], v[114:115]
	s_cmp_eq_u32 s22, 1
	s_cbranch_scc1 .Lp2_nopf
	v_lshl_add_u64 v[54:55], v[96:97], 0, s[20:21]
	v_lshl_add_u64 v[54:55], v[54:55], 0, s[58:59]
	v_add_co_u32_e32 v56, vcc, s65, v54
	s_nop 1
	v_addc_co_u32_e32 v57, vcc, 0, v55, vcc
	v_add_co_u32_e32 v58, vcc, s66, v54
	s_nop 1
	v_addc_co_u32_e32 v59, vcc, 0, v55, vcc
	global_load_dwordx4 v[196:199], v[56:57], off
	global_load_dwordx4 v[200:203], v[58:59], off
	v_add_co_u32_e32 v56, vcc, s67, v54
	s_nop 1
	v_addc_co_u32_e32 v57, vcc, 0, v55, vcc
	v_add_co_u32_e32 v58, vcc, s68, v54
	s_nop 1
	v_addc_co_u32_e32 v59, vcc, 0, v55, vcc
	global_load_dwordx4 v[204:207], v[56:57], off
	global_load_dwordx4 v[208:211], v[58:59], off
	v_add_co_u32_e32 v56, vcc, s69, v54
	s_nop 1
	v_addc_co_u32_e32 v57, vcc, 0, v55, vcc
	v_add_co_u32_e32 v58, vcc, s70, v54
	s_nop 1
	v_addc_co_u32_e32 v59, vcc, 0, v55, vcc
	global_load_dwordx4 v[212:215], v[56:57], off
	global_load_dwordx4 v[216:219], v[58:59], off
	v_add_co_u32_e32 v56, vcc, s71, v54
	s_nop 1
	v_addc_co_u32_e32 v57, vcc, 0, v55, vcc
	v_add_co_u32_e32 v58, vcc, s72, v54
	s_nop 1
	v_addc_co_u32_e32 v59, vcc, 0, v55, vcc
	global_load_dwordx4 v[220:223], v[56:57], off
	global_load_dwordx4 v[224:227], v[58:59], off
	v_lshl_add_u64 v[54:55], v[94:95], 0, s[20:21]
	v_lshl_add_u64 v[54:55], v[54:55], 0, s[58:59]
	v_add_co_u32_e32 v56, vcc, s73, v54
	s_nop 1
	v_addc_co_u32_e32 v57, vcc, 0, v55, vcc
	global_load_dwordx2 v[228:229], v[56:57], off
	v_add_co_u32_e32 v58, vcc, s75, v54
	s_nop 1
	v_addc_co_u32_e32 v59, vcc, 0, v55, vcc
	global_load_dwordx2 v[230:231], v[58:59], off
	v_lshl_add_u64 v[54:55], v[98:99], 0, s[20:21]
	v_lshl_add_u64 v[54:55], v[54:55], 0, s[58:59]
	global_load_dwordx4 v[232:235], v[54:55], off offset:-256
	global_load_dwordx4 v[236:239], v[54:55], off offset:-192
	global_load_dwordx4 v[240:243], v[54:55], off offset:-128
	global_load_dwordx4 v[244:247], v[54:55], off offset:-64
	global_load_dwordx4 v[248:251], v[54:55], off
	global_load_dwordx4 v[104:107], v[54:55], off offset:64
	global_load_dwordx4 v[108:111], v[54:55], off offset:128
	global_load_dwordx4 v[112:115], v[54:55], off offset:192
.Lp2_nopf:
	s_andn2_b64 vcc, exec, s[26:27]
	ds_write_b16 v101, v186
	ds_write_b16_d16_hi v101, v186 offset:272
	ds_write_b16 v101, v187 offset:544
	ds_write_b16_d16_hi v101, v187 offset:816
	v_lshlrev_b32_e32 v3, 16, v186
	v_and_b32_e32 v54, 0xffff0000, v186
	v_lshlrev_b32_e32 v55, 16, v187
	v_mul_f32_e32 v3, v172, v3
	v_mul_f32_e32 v54, v172, v54
	v_mul_f32_e32 v55, v172, v55
	v_bfe_u32 v56, v3, 16, 1
	v_bfe_u32 v57, v54, 16, 1
	v_bfe_u32 v58, v55, 16, 1
	v_add3_u32 v3, v3, v56, s74
	v_add3_u32 v54, v54, v57, s74
	v_add3_u32 v55, v55, v58, s74
	ds_write_b16_d16_hi v102, v3
	ds_write_b16_d16_hi v102, v54 offset:272
	ds_write_b16_d16_hi v102, v55 offset:544
	v_and_b32_e32 v3, 0xffff0000, v187
	v_mul_f32_e32 v3, v172, v3
	v_bfe_u32 v54, v3, 16, 1
	v_add3_u32 v3, v3, v54, s74
	ds_write_b16_d16_hi v102, v3 offset:816
	ds_write_b16 v101, v4 offset:128
	ds_write_b16_d16_hi v101, v4 offset:400
	ds_write_b16 v101, v5 offset:672
	ds_write_b16_d16_hi v101, v5 offset:944
	v_lshlrev_b32_e32 v3, 16, v4
	v_mul_f32_e32 v3, v173, v3
	v_bfe_u32 v54, v3, 16, 1
	v_add3_u32 v3, v3, v54, s74
	ds_write_b16_d16_hi v102, v3 offset:128
	v_and_b32_e32 v3, 0xffff0000, v4
	v_mul_f32_e32 v3, v173, v3
	v_bfe_u32 v4, v3, 16, 1
	v_add3_u32 v3, v3, v4, s74
	ds_write_b16_d16_hi v102, v3 offset:400
	v_lshlrev_b32_e32 v3, 16, v5
	v_mul_f32_e32 v3, v173, v3
	v_bfe_u32 v4, v3, 16, 1
	v_add3_u32 v3, v3, v4, s74
	ds_write_b16_d16_hi v102, v3 offset:672
	v_and_b32_e32 v3, 0xffff0000, v5
	v_mul_f32_e32 v3, v173, v3
	v_bfe_u32 v4, v3, 16, 1
	v_add3_u32 v3, v3, v4, s74
	ds_write_b16_d16_hi v102, v3 offset:944
	v_cndmask_b32_e64 v3, 0, 1, s[26:27]
	v_cmp_ne_u32_e64 s[12:13], 1, v3
	v_mov_b32_e32 v57, 0
	v_mov_b32_e32 v56, 0
	v_mov_b32_e32 v55, 0
	v_mov_b32_e32 v54, 0
	s_waitcnt lgkmcnt(0)
	s_barrier
	s_cbranch_vccnz .LBB0_267
	ds_read_b128 v[54:57], v154
	ds_read_b128 v[58:61], v154 offset:4096
	ds_read_b128 v[62:65], v155
	ds_read_b128 v[66:69], v155 offset:4096
	s_andn2_b64 vcc, exec, s[2:3]
	s_waitcnt lgkmcnt(3)
	v_mfma_f32_16x16x32_bf16 v[54:57], v[54:57], v[50:53], 0
	s_waitcnt lgkmcnt(2)
	v_mfma_f32_16x16x32_bf16 v[58:61], v[58:61], v[50:53], 0
	s_waitcnt lgkmcnt(1)
	v_mfma_f32_16x16x32_bf16 v[54:57], v[62:65], v[46:49], v[54:57]
	ds_read_b128 v[62:65], v156
	s_waitcnt lgkmcnt(1)
	v_mfma_f32_16x16x32_bf16 v[58:61], v[66:69], v[46:49], v[58:61]
	ds_read_b128 v[66:69], v156 offset:4096
	s_waitcnt lgkmcnt(1)
	v_mfma_f32_16x16x32_bf16 v[54:57], v[62:65], v[42:45], v[54:57]
	ds_read_b128 v[62:65], v157
	s_waitcnt lgkmcnt(1)
	v_mfma_f32_16x16x32_bf16 v[58:61], v[66:69], v[42:45], v[58:61]
	ds_read_b128 v[66:69], v157 offset:4096
	s_waitcnt lgkmcnt(1)
	v_mfma_f32_16x16x32_bf16 v[54:57], v[62:65], v[38:41], v[54:57]
	s_waitcnt lgkmcnt(0)
	v_mfma_f32_16x16x32_bf16 v[58:61], v[66:69], v[38:41], v[58:61]
	ds_read_b128 v[62:65], v154 offset:32768
	ds_read_b128 v[66:69], v154 offset:36864
	s_waitcnt lgkmcnt(1)
	v_mfma_f32_16x16x32_bf16 v[54:57], v[62:65], v[34:37], v[54:57]
	ds_read_b128 v[62:65], v155 offset:32768
	ds_read_b128 v[70:73], v155 offset:36864
	s_waitcnt lgkmcnt(1)
	v_mfma_f32_16x16x32_bf16 v[54:57], v[62:65], v[30:33], v[54:57]
	ds_read_b128 v[62:65], v156 offset:32768
	ds_read_b128 v[174:177], v156 offset:36864
	s_waitcnt lgkmcnt(1)
	v_mfma_f32_16x16x32_bf16 v[54:57], v[62:65], v[26:29], v[54:57]
	ds_read_b128 v[62:65], v157 offset:32768
	ds_read_b128 v[178:181], v157 offset:36864
	v_mfma_f32_16x16x32_bf16 v[58:61], v[66:69], v[34:37], v[58:61]
	s_waitcnt lgkmcnt(1)
	v_mfma_f32_16x16x32_bf16 v[54:57], v[62:65], v[22:25], v[54:57]
	v_mfma_f32_16x16x32_bf16 v[58:61], v[70:73], v[30:33], v[58:61]
	s_nop 6
	v_mul_f32_e32 v3, v54, v160
	v_mul_f32_e32 v5, v56, v160
	v_mul_f32_e32 v54, v57, v160
	v_mfma_f32_16x16x32_bf16 v[56:59], v[174:177], v[26:29], v[58:61]
	v_mul_f32_e32 v4, v55, v160
	v_mul_f32_e32 v3, v3, v168
	v_mul_f32_e32 v4, v4, v169
	s_waitcnt lgkmcnt(0)
	v_mfma_f32_16x16x32_bf16 v[58:61], v[178:181], v[22:25], v[56:59]
	v_mul_f32_e32 v5, v5, v170
	v_mul_f32_e32 v55, v54, v171
	s_cbranch_vccnz .LBB0_263
	v_cndmask_b32_e64 v3, 0, v3, s[4:5]
	v_cndmask_b32_e64 v4, 0, v4, s[6:7]
	v_cndmask_b32_e64 v5, 0, v5, s[8:9]
	v_cndmask_b32_e64 v55, 0, v55, s[10:11]

.LBB0_267:
	v_cndmask_b32_e64 v3, 0, 1, s[30:31]
	v_mov_b32_e32 v61, 0
	v_cmp_ne_u32_e64 s[14:15], 1, v3
	s_andn2_b64 vcc, exec, s[30:31]
	v_mov_b32_e32 v60, 0
	v_mov_b32_e32 v59, 0
	v_mov_b32_e32 v58, 0
	s_cbranch_vccnz .LBB0_274
	ds_read_b128 v[58:61], v154 offset:8192
	ds_read_b128 v[62:65], v154 offset:12288
	ds_read_b128 v[66:69], v155 offset:8192
	ds_read_b128 v[70:73], v155 offset:12288
	s_andn2_b64 vcc, exec, s[34:35]
	s_waitcnt lgkmcnt(3)
	v_mfma_f32_16x16x32_bf16 v[58:61], v[58:61], v[50:53], 0
	s_waitcnt lgkmcnt(2)
	v_mfma_f32_16x16x32_bf16 v[62:65], v[62:65], v[50:53], 0
	s_waitcnt lgkmcnt(1)
	v_mfma_f32_16x16x32_bf16 v[58:61], v[66:69], v[46:49], v[58:61]
	ds_read_b128 v[66:69], v156 offset:8192
	s_waitcnt lgkmcnt(1)
	v_mfma_f32_16x16x32_bf16 v[62:65], v[70:73], v[46:49], v[62:65]
	ds_read_b128 v[70:73], v156 offset:12288
	s_waitcnt lgkmcnt(1)
	v_mfma_f32_16x16x32_bf16 v[58:61], v[66:69], v[42:45], v[58:61]
	ds_read_b128 v[66:69], v157 offset:8192
	s_waitcnt lgkmcnt(1)
	v_mfma_f32_16x16x32_bf16 v[62:65], v[70:73], v[42:45], v[62:65]
	ds_read_b128 v[70:73], v157 offset:12288
	s_waitcnt lgkmcnt(1)
	v_mfma_f32_16x16x32_bf16 v[58:61], v[66:69], v[38:41], v[58:61]
	s_waitcnt lgkmcnt(0)
	v_mfma_f32_16x16x32_bf16 v[62:65], v[70:73], v[38:41], v[62:65]
	ds_read_b128 v[66:69], v154 offset:40960
	ds_read_b128 v[70:73], v154 offset:45056
	s_waitcnt lgkmcnt(1)
	v_mfma_f32_16x16x32_bf16 v[58:61], v[66:69], v[34:37], v[58:61]
	ds_read_b128 v[66:69], v155 offset:40960
	ds_read_b128 v[174:177], v155 offset:45056
	s_waitcnt lgkmcnt(1)
	v_mfma_f32_16x16x32_bf16 v[58:61], v[66:69], v[30:33], v[58:61]
	ds_read_b128 v[66:69], v156 offset:40960
	ds_read_b128 v[178:181], v156 offset:45056
	s_waitcnt lgkmcnt(1)
	v_mfma_f32_16x16x32_bf16 v[58:61], v[66:69], v[26:29], v[58:61]
	ds_read_b128 v[66:69], v157 offset:40960
	ds_read_b128 v[182:185], v157 offset:45056
	v_mfma_f32_16x16x32_bf16 v[62:65], v[70:73], v[34:37], v[62:65]
	s_waitcnt lgkmcnt(1)
	v_mfma_f32_16x16x32_bf16 v[58:61], v[66:69], v[22:25], v[58:61]
	v_mfma_f32_16x16x32_bf16 v[62:65], v[174:177], v[30:33], v[62:65]
	s_nop 6
	v_mul_f32_e32 v3, v58, v162
	v_mul_f32_e32 v5, v60, v162
	v_mul_f32_e32 v58, v61, v162
	v_mfma_f32_16x16x32_bf16 v[60:63], v[178:181], v[26:29], v[62:65]
	v_mul_f32_e32 v4, v59, v162
	v_mul_f32_e32 v3, v3, v168
	v_mul_f32_e32 v4, v4, v169
	s_waitcnt lgkmcnt(0)
	v_mfma_f32_16x16x32_bf16 v[62:65], v[182:185], v[22:25], v[60:63]
	v_mul_f32_e32 v5, v5, v170
	v_mul_f32_e32 v59, v58, v171
	s_cbranch_vccnz .LBB0_270
	v_cndmask_b32_e64 v3, 0, v3, s[4:5]
	v_cndmask_b32_e64 v4, 0, v4, s[6:7]
	v_cndmask_b32_e64 v5, 0, v5, s[8:9]
	v_cndmask_b32_e64 v59, 0, v59, s[10:11]

.LBB0_274:
	v_cndmask_b32_e64 v3, 0, 1, s[40:41]
	v_mov_b32_e32 v65, 0
	v_cmp_ne_u32_e64 s[16:17], 1, v3
	s_andn2_b64 vcc, exec, s[40:41]
	v_mov_b32_e32 v64, 0
	v_mov_b32_e32 v63, 0
	v_mov_b32_e32 v62, 0
	s_cbranch_vccnz .LBB0_281
	ds_read_b128 v[62:65], v154 offset:16384
	ds_read_b128 v[66:69], v154 offset:20480
	ds_read_b128 v[70:73], v155 offset:16384
	ds_read_b128 v[174:177], v155 offset:20480
	s_andn2_b64 vcc, exec, s[42:43]
	s_waitcnt lgkmcnt(3)
	v_mfma_f32_16x16x32_bf16 v[62:65], v[62:65], v[50:53], 0
	s_waitcnt lgkmcnt(2)
	v_mfma_f32_16x16x32_bf16 v[66:69], v[66:69], v[50:53], 0
	s_waitcnt lgkmcnt(1)
	v_mfma_f32_16x16x32_bf16 v[62:65], v[70:73], v[46:49], v[62:65]
	ds_read_b128 v[70:73], v156 offset:16384
	s_waitcnt lgkmcnt(1)
	v_mfma_f32_16x16x32_bf16 v[66:69], v[174:177], v[46:49], v[66:69]
	ds_read_b128 v[174:177], v156 offset:20480
	s_waitcnt lgkmcnt(1)
	v_mfma_f32_16x16x32_bf16 v[62:65], v[70:73], v[42:45], v[62:65]
	ds_read_b128 v[70:73], v157 offset:16384
	s_waitcnt lgkmcnt(1)
	v_mfma_f32_16x16x32_bf16 v[66:69], v[174:177], v[42:45], v[66:69]
	ds_read_b128 v[174:177], v157 offset:20480
	s_waitcnt lgkmcnt(1)
	v_mfma_f32_16x16x32_bf16 v[62:65], v[70:73], v[38:41], v[62:65]
	s_waitcnt lgkmcnt(0)
	v_mfma_f32_16x16x32_bf16 v[66:69], v[174:177], v[38:41], v[66:69]
	ds_read_b128 v[70:73], v154 offset:49152
	ds_read_b128 v[174:177], v154 offset:53248
	s_waitcnt lgkmcnt(1)
	v_mfma_f32_16x16x32_bf16 v[62:65], v[70:73], v[34:37], v[62:65]
	ds_read_b128 v[70:73], v155 offset:49152
	ds_read_b128 v[178:181], v155 offset:53248
	s_waitcnt lgkmcnt(1)
	v_mfma_f32_16x16x32_bf16 v[62:65], v[70:73], v[30:33], v[62:65]
	ds_read_b128 v[70:73], v156 offset:49152
	ds_read_b128 v[182:185], v156 offset:53248
	s_waitcnt lgkmcnt(1)
	v_mfma_f32_16x16x32_bf16 v[62:65], v[70:73], v[26:29], v[62:65]
	ds_read_b128 v[70:73], v157 offset:49152
	ds_read_b128 v[186:189], v157 offset:53248
	v_mfma_f32_16x16x32_bf16 v[66:69], v[174:177], v[34:37], v[66:69]
	s_waitcnt lgkmcnt(1)
	v_mfma_f32_16x16x32_bf16 v[62:65], v[70:73], v[22:25], v[62:65]
	v_mfma_f32_16x16x32_bf16 v[66:69], v[178:181], v[30:33], v[66:69]
	s_nop 6
	v_mul_f32_e32 v3, v62, v164
	v_mul_f32_e32 v5, v64, v164
	v_mul_f32_e32 v62, v65, v164
	v_mfma_f32_16x16x32_bf16 v[64:67], v[182:185], v[26:29], v[66:69]
	v_mul_f32_e32 v4, v63, v164
	v_mul_f32_e32 v3, v3, v168
	v_mul_f32_e32 v4, v4, v169
	s_waitcnt lgkmcnt(0)
	v_mfma_f32_16x16x32_bf16 v[66:69], v[186:189], v[22:25], v[64:67]
	v_mul_f32_e32 v5, v5, v170
	v_mul_f32_e32 v63, v62, v171
	s_cbranch_vccnz .LBB0_277
	v_cndmask_b32_e64 v3, 0, v3, s[4:5]
	v_cndmask_b32_e64 v4, 0, v4, s[6:7]
	v_cndmask_b32_e64 v5, 0, v5, s[8:9]
	v_cndmask_b32_e64 v63, 0, v63, s[10:11]

.LBB0_281:
	v_cndmask_b32_e64 v3, 0, 1, s[48:49]
	v_mov_b32_e32 v69, 0
	v_cmp_ne_u32_e64 s[18:19], 1, v3
	s_andn2_b64 vcc, exec, s[48:49]
	v_mov_b32_e32 v68, 0
	v_mov_b32_e32 v67, 0
	v_mov_b32_e32 v66, 0
	s_cbranch_vccnz .LBB0_288
	ds_read_b128 v[66:69], v154 offset:24576
	ds_read_b128 v[70:73], v154 offset:28672
	ds_read_b128 v[174:177], v155 offset:24576
	ds_read_b128 v[178:181], v155 offset:28672
	s_andn2_b64 vcc, exec, s[50:51]
	s_waitcnt lgkmcnt(3)
	v_mfma_f32_16x16x32_bf16 v[66:69], v[66:69], v[50:53], 0
	s_waitcnt lgkmcnt(2)
	v_mfma_f32_16x16x32_bf16 v[70:73], v[70:73], v[50:53], 0
	s_waitcnt lgkmcnt(1)
	v_mfma_f32_16x16x32_bf16 v[66:69], v[174:177], v[46:49], v[66:69]
	ds_read_b128 v[174:177], v156 offset:24576
	s_waitcnt lgkmcnt(1)
	v_mfma_f32_16x16x32_bf16 v[70:73], v[178:181], v[46:49], v[70:73]
	ds_read_b128 v[178:181], v156 offset:28672
	s_waitcnt lgkmcnt(1)
	v_mfma_f32_16x16x32_bf16 v[66:69], v[174:177], v[42:45], v[66:69]
	ds_read_b128 v[174:177], v157 offset:24576
	s_waitcnt lgkmcnt(1)
	v_mfma_f32_16x16x32_bf16 v[70:73], v[178:181], v[42:45], v[70:73]
	ds_read_b128 v[178:181], v157 offset:28672
	s_waitcnt lgkmcnt(1)
	v_mfma_f32_16x16x32_bf16 v[66:69], v[174:177], v[38:41], v[66:69]
	s_waitcnt lgkmcnt(0)
	v_mfma_f32_16x16x32_bf16 v[70:73], v[178:181], v[38:41], v[70:73]
	ds_read_b128 v[174:177], v154 offset:57344
	ds_read_b128 v[178:181], v154 offset:61440
	s_waitcnt lgkmcnt(1)
	v_mfma_f32_16x16x32_bf16 v[66:69], v[174:177], v[34:37], v[66:69]
	ds_read_b128 v[174:177], v155 offset:57344
	ds_read_b128 v[182:185], v155 offset:61440
	s_waitcnt lgkmcnt(1)
	v_mfma_f32_16x16x32_bf16 v[66:69], v[174:177], v[30:33], v[66:69]
	ds_read_b128 v[174:177], v156 offset:57344
	ds_read_b128 v[186:189], v156 offset:61440
	s_waitcnt lgkmcnt(1)
	v_mfma_f32_16x16x32_bf16 v[66:69], v[174:177], v[26:29], v[66:69]
	ds_read_b128 v[174:177], v157 offset:57344
	ds_read_b128 v[190:193], v157 offset:61440
	v_mfma_f32_16x16x32_bf16 v[70:73], v[178:181], v[34:37], v[70:73]
	s_waitcnt lgkmcnt(1)
	v_mfma_f32_16x16x32_bf16 v[66:69], v[174:177], v[22:25], v[66:69]
	v_mfma_f32_16x16x32_bf16 v[70:73], v[182:185], v[30:33], v[70:73]
	s_nop 6
	v_mul_f32_e32 v3, v66, v166
	v_mul_f32_e32 v5, v68, v166
	v_mul_f32_e32 v66, v69, v166
	v_mfma_f32_16x16x32_bf16 v[68:71], v[186:189], v[26:29], v[70:73]
	v_mul_f32_e32 v4, v67, v166
	v_mul_f32_e32 v3, v3, v168
	v_mul_f32_e32 v4, v4, v169
	s_waitcnt lgkmcnt(0)
	v_mfma_f32_16x16x32_bf16 v[70:73], v[190:193], v[22:25], v[68:71]
	v_mul_f32_e32 v5, v5, v170
	v_mul_f32_e32 v67, v66, v171
	s_cbranch_vccnz .LBB0_284
	v_cndmask_b32_e64 v3, 0, v3, s[4:5]
	v_cndmask_b32_e64 v4, 0, v4, s[6:7]
	v_cndmask_b32_e64 v5, 0, v5, s[8:9]
	v_cndmask_b32_e64 v67, 0, v67, s[10:11]

.LBB0_454:
	ds_read_b128 v[162:165], v158
	ds_read_b128 v[166:169], v158 offset:1024
	ds_read_b128 v[170:173], v158 offset:2048
	ds_read_b128 v[174:177], v158 offset:3072
	ds_read_b128 v[178:181], v159
	ds_read_b128 v[182:185], v159 offset:1024
	ds_read_b128 v[186:189], v159 offset:2048
	ds_read_b128 v[190:193], v159 offset:3072
	s_add_u32 s44, s38, s42
	s_addc_u32 s45, s39, s43
	s_add_u32 s46, s44, 0x100
	s_addc_u32 s47, s45, 0
	s_add_u32 s70, s67, s42
	s_addc_u32 s71, s68, s43
	s_cmp_eq_u32 s42, 0
	s_cselect_b64 s[44:45], -1, 0
	s_and_b64 s[44:45], s[40:41], s[44:45]
	s_cmpk_eq_i32 s42, 0x1f00
	v_cndmask_b32_e64 v149, 0, 1, s[44:45]
	s_cselect_b32 s47, s29, s47
	s_cselect_b32 s46, s65, s46
	v_readfirstlane_b32 s72, v149
	s_cselect_b32 s45, s27, s71
	s_cselect_b32 s44, s66, s70
	v_lshl_add_u64 v[226:227], v[150:151], 0, s[42:43]
	s_add_i32 m0, s53, 0xc000
	ds_read_b128 v[194:197], v160
	ds_read_b128 v[198:201], v160 offset:1024
	ds_read_b128 v[202:205], v160 offset:2048
	ds_read_b128 v[206:209], v160 offset:3072
	ds_read_b128 v[210:213], v160 offset:4096
	ds_read_b128 v[214:217], v160 offset:5120
	ds_read_b128 v[218:221], v160 offset:6144
	ds_read_b128 v[222:225], v160 offset:7168
	global_load_lds_dwordx4 v[226:227], off
	v_lshl_add_u64 v[226:227], v[152:153], 0, s[42:43]
	s_add_i32 m0, s53, 0xe000
	s_and_b32 s72, s72, 1
	global_load_lds_dwordx4 v[226:227], off
	s_cmp_lg_u32 s72, 0
	s_cbranch_scc1 .Lpg8r2
	s_waitcnt vmcnt(8)
	s_branch .Lpg8e2

.Lpg8e2:
	s_waitcnt lgkmcnt(0)
	s_barrier
	s_setprio 1
	s_waitcnt lgkmcnt(0)
	v_mfma_f32_16x16x32_bf16 v[126:129], v[162:165], v[194:197], v[126:129]
	v_mfma_f32_16x16x32_bf16 v[122:125], v[170:173], v[194:197], v[122:125]
	v_mfma_f32_16x16x32_bf16 v[110:113], v[162:165], v[202:205], v[110:113]
	v_mfma_f32_16x16x32_bf16 v[106:109], v[170:173], v[202:205], v[106:109]
	v_mfma_f32_16x16x32_bf16 v[94:97], v[162:165], v[210:213], v[94:97]
	v_mfma_f32_16x16x32_bf16 v[90:93], v[170:173], v[210:213], v[90:93]
	v_mfma_f32_16x16x32_bf16 v[78:81], v[162:165], v[218:221], v[78:81]
	v_mfma_f32_16x16x32_bf16 v[74:77], v[170:173], v[218:221], v[74:77]
	v_mfma_f32_16x16x32_bf16 v[126:129], v[166:169], v[198:201], v[126:129]
	v_mfma_f32_16x16x32_bf16 v[122:125], v[174:177], v[198:201], v[122:125]
	v_mfma_f32_16x16x32_bf16 v[110:113], v[166:169], v[206:209], v[110:113]
	v_mfma_f32_16x16x32_bf16 v[106:109], v[174:177], v[206:209], v[106:109]
	v_mfma_f32_16x16x32_bf16 v[94:97], v[166:169], v[214:217], v[94:97]
	v_mfma_f32_16x16x32_bf16 v[90:93], v[174:177], v[214:217], v[90:93]
	v_mfma_f32_16x16x32_bf16 v[78:81], v[166:169], v[222:225], v[78:81]
	v_mfma_f32_16x16x32_bf16 v[74:77], v[174:177], v[222:225], v[74:77]
	s_setprio 0
	s_setprio 1
	v_mfma_f32_16x16x32_bf16 v[118:121], v[178:181], v[194:197], v[118:121]
	v_mfma_f32_16x16x32_bf16 v[114:117], v[186:189], v[194:197], v[114:117]
	v_mfma_f32_16x16x32_bf16 v[102:105], v[178:181], v[202:205], v[102:105]
	v_mfma_f32_16x16x32_bf16 v[98:101], v[186:189], v[202:205], v[98:101]
	v_mfma_f32_16x16x32_bf16 v[86:89], v[178:181], v[210:213], v[86:89]
	v_mfma_f32_16x16x32_bf16 v[82:85], v[186:189], v[210:213], v[82:85]
	v_mfma_f32_16x16x32_bf16 v[70:73], v[178:181], v[218:221], v[70:73]
	v_mfma_f32_16x16x32_bf16 v[66:69], v[186:189], v[218:221], v[66:69]
	v_mfma_f32_16x16x32_bf16 v[118:121], v[182:185], v[198:201], v[118:121]
	v_mfma_f32_16x16x32_bf16 v[114:117], v[190:193], v[198:201], v[114:117]
	v_mfma_f32_16x16x32_bf16 v[102:105], v[182:185], v[206:209], v[102:105]
	v_mfma_f32_16x16x32_bf16 v[98:101], v[190:193], v[206:209], v[98:101]
	v_mfma_f32_16x16x32_bf16 v[86:89], v[182:185], v[214:217], v[86:89]
	v_mfma_f32_16x16x32_bf16 v[82:85], v[190:193], v[214:217], v[82:85]
	v_mfma_f32_16x16x32_bf16 v[70:73], v[182:185], v[222:225], v[70:73]
	v_mfma_f32_16x16x32_bf16 v[66:69], v[190:193], v[222:225], v[66:69]
	s_setprio 0
	s_barrier
	s_add_i32 s70, s93, s52
	v_lshl_add_u64 v[226:227], s[44:45], 0, v[132:133]
	s_mov_b32 m0, s70
	ds_read_b128 v[194:197], v160 offset:16384
	ds_read_b128 v[198:201], v160 offset:17408
	ds_read_b128 v[202:205], v160 offset:18432
	ds_read_b128 v[206:209], v160 offset:19456
	ds_read_b128 v[210:213], v160 offset:20480
	ds_read_b128 v[214:217], v160 offset:21504
	ds_read_b128 v[218:221], v160 offset:22528
	ds_read_b128 v[222:225], v160 offset:23552
	global_load_lds_dwordx4 v[226:227], off
	s_add_i32 m0, s70, 0x2000
	s_add_u32 s70, s44, 0x100000
	v_lshl_add_u64 v[228:229], s[44:45], 0, v[136:137]
	s_addc_u32 s71, s45, 0
	s_add_i32 s73, s63, s52
	global_load_lds_dwordx4 v[228:229], off
	v_lshl_add_u64 v[230:231], s[70:71], 0, v[132:133]
	s_mov_b32 m0, s73
	v_lshl_add_u64 v[232:233], s[46:47], 0, v[134:135]
	global_load_lds_dwordx4 v[230:231], off
	v_lshl_add_u64 v[230:231], s[70:71], 0, v[136:137]
	s_add_i32 m0, s73, 0x2000
	s_nop 0
	global_load_lds_dwordx4 v[230:231], off
	v_lshl_add_u64 v[230:231], s[46:47], 0, v[130:131]
	s_mov_b32 m0, s53
	s_nop 0
	global_load_lds_dwordx4 v[230:231], off
	s_mov_b32 m0, s54
	s_nop 0
	global_load_lds_dwordx4 v[232:233], off
	s_cmp_lg_u32 s72, 0
	s_cbranch_scc1 .Lpg8r3
	s_waitcnt vmcnt(8)
	s_branch .Lpg8e3

.Lpg8e3:
	s_waitcnt lgkmcnt(0)
	s_barrier
	s_setprio 1
	s_waitcnt lgkmcnt(0)
	v_mfma_f32_16x16x32_bf16 v[62:65], v[162:165], v[194:197], v[62:65]
	v_mfma_f32_16x16x32_bf16 v[58:61], v[170:173], v[194:197], v[58:61]
	v_mfma_f32_16x16x32_bf16 v[46:49], v[162:165], v[202:205], v[46:49]
	v_mfma_f32_16x16x32_bf16 v[42:45], v[170:173], v[202:205], v[42:45]
	v_mfma_f32_16x16x32_bf16 v[30:33], v[162:165], v[210:213], v[30:33]
	v_mfma_f32_16x16x32_bf16 v[26:29], v[170:173], v[210:213], v[26:29]
	v_mfma_f32_16x16x32_bf16 v[14:17], v[162:165], v[218:221], v[14:17]
	v_mfma_f32_16x16x32_bf16 v[10:13], v[170:173], v[218:221], v[10:13]
	v_mfma_f32_16x16x32_bf16 v[62:65], v[166:169], v[198:201], v[62:65]
	v_mfma_f32_16x16x32_bf16 v[58:61], v[174:177], v[198:201], v[58:61]
	v_mfma_f32_16x16x32_bf16 v[46:49], v[166:169], v[206:209], v[46:49]
	v_mfma_f32_16x16x32_bf16 v[42:45], v[174:177], v[206:209], v[42:45]
	v_mfma_f32_16x16x32_bf16 v[30:33], v[166:169], v[214:217], v[30:33]
	v_mfma_f32_16x16x32_bf16 v[26:29], v[174:177], v[214:217], v[26:29]
	v_mfma_f32_16x16x32_bf16 v[14:17], v[166:169], v[222:225], v[14:17]
	v_mfma_f32_16x16x32_bf16 v[10:13], v[174:177], v[222:225], v[10:13]
	s_setprio 0
	s_setprio 1
	v_mfma_f32_16x16x32_bf16 v[54:57], v[178:181], v[194:197], v[54:57]
	v_mfma_f32_16x16x32_bf16 v[50:53], v[186:189], v[194:197], v[50:53]
	v_mfma_f32_16x16x32_bf16 v[38:41], v[178:181], v[202:205], v[38:41]
	v_mfma_f32_16x16x32_bf16 v[34:37], v[186:189], v[202:205], v[34:37]
	v_mfma_f32_16x16x32_bf16 v[22:25], v[178:181], v[210:213], v[22:25]
	v_mfma_f32_16x16x32_bf16 v[18:21], v[186:189], v[210:213], v[18:21]
	v_mfma_f32_16x16x32_bf16 v[6:9], v[178:181], v[218:221], v[6:9]
	v_mfma_f32_16x16x32_bf16 v[2:5], v[186:189], v[218:221], v[2:5]
	v_mfma_f32_16x16x32_bf16 v[54:57], v[182:185], v[198:201], v[54:57]
	v_mfma_f32_16x16x32_bf16 v[50:53], v[190:193], v[198:201], v[50:53]
	v_mfma_f32_16x16x32_bf16 v[38:41], v[182:185], v[206:209], v[38:41]
	v_mfma_f32_16x16x32_bf16 v[34:37], v[190:193], v[206:209], v[34:37]
	v_mfma_f32_16x16x32_bf16 v[22:25], v[182:185], v[214:217], v[22:25]
	v_mfma_f32_16x16x32_bf16 v[18:21], v[190:193], v[214:217], v[18:21]
	v_mfma_f32_16x16x32_bf16 v[6:9], v[182:185], v[222:225], v[6:9]
	v_mfma_f32_16x16x32_bf16 v[2:5], v[190:193], v[222:225], v[2:5]
	s_setprio 0
	s_barrier
	s_add_i32 s70, 0, 0x18000
	v_add_u32_e32 v149, s70, v156
	s_add_i32 s71, 0, 0x1c000
	ds_read_b128 v[162:165], v149
	ds_read_b128 v[166:169], v149 offset:1024
	ds_read_b128 v[170:173], v149 offset:2048
	ds_read_b128 v[174:177], v149 offset:3072
	v_add_u32_e32 v149, s71, v156
	ds_read_b128 v[178:181], v149
	ds_read_b128 v[182:185], v149 offset:1024
	ds_read_b128 v[186:189], v149 offset:2048
	ds_read_b128 v[190:193], v149 offset:3072
	s_add_u32 s46, s46, 0x100000
	s_addc_u32 s47, s47, 0
	s_mov_b32 m0, s55
	v_lshl_add_u64 v[234:235], s[46:47], 0, v[130:131]
	ds_read_b128 v[194:197], v160 offset:32768
	ds_read_b128 v[198:201], v160 offset:33792
	ds_read_b128 v[202:205], v160 offset:34816
	ds_read_b128 v[206:209], v160 offset:35840
	ds_read_b128 v[210:213], v160 offset:36864
	ds_read_b128 v[214:217], v160 offset:37888
	ds_read_b128 v[218:221], v160 offset:38912
	ds_read_b128 v[222:225], v160 offset:39936
	global_load_lds_dwordx4 v[234:235], off
	v_lshl_add_u64 v[234:235], s[46:47], 0, v[134:135]
	s_mov_b32 m0, s56
	s_nop 0
	global_load_lds_dwordx4 v[234:235], off
	s_waitcnt vmcnt(8)
	s_waitcnt lgkmcnt(0)
	s_barrier
	s_setprio 1
	s_waitcnt lgkmcnt(0)
	v_mfma_f32_16x16x32_bf16 v[126:129], v[162:165], v[194:197], v[126:129]
	v_mfma_f32_16x16x32_bf16 v[122:125], v[170:173], v[194:197], v[122:125]
	v_mfma_f32_16x16x32_bf16 v[110:113], v[162:165], v[202:205], v[110:113]
	v_mfma_f32_16x16x32_bf16 v[106:109], v[170:173], v[202:205], v[106:109]
	v_mfma_f32_16x16x32_bf16 v[94:97], v[162:165], v[210:213], v[94:97]
	v_mfma_f32_16x16x32_bf16 v[90:93], v[170:173], v[210:213], v[90:93]
	v_mfma_f32_16x16x32_bf16 v[78:81], v[162:165], v[218:221], v[78:81]
	v_mfma_f32_16x16x32_bf16 v[74:77], v[170:173], v[218:221], v[74:77]
	v_mfma_f32_16x16x32_bf16 v[126:129], v[166:169], v[198:201], v[126:129]
	v_mfma_f32_16x16x32_bf16 v[122:125], v[174:177], v[198:201], v[122:125]
	v_mfma_f32_16x16x32_bf16 v[110:113], v[166:169], v[206:209], v[110:113]
	v_mfma_f32_16x16x32_bf16 v[106:109], v[174:177], v[206:209], v[106:109]
	v_mfma_f32_16x16x32_bf16 v[94:97], v[166:169], v[214:217], v[94:97]
	v_mfma_f32_16x16x32_bf16 v[90:93], v[174:177], v[214:217], v[90:93]
	v_mfma_f32_16x16x32_bf16 v[78:81], v[166:169], v[222:225], v[78:81]
	v_mfma_f32_16x16x32_bf16 v[74:77], v[174:177], v[222:225], v[74:77]
	s_setprio 0
	s_setprio 1
	v_mfma_f32_16x16x32_bf16 v[118:121], v[178:181], v[194:197], v[118:121]
	v_mfma_f32_16x16x32_bf16 v[114:117], v[186:189], v[194:197], v[114:117]
	v_mfma_f32_16x16x32_bf16 v[102:105], v[178:181], v[202:205], v[102:105]
	v_mfma_f32_16x16x32_bf16 v[98:101], v[186:189], v[202:205], v[98:101]
	v_mfma_f32_16x16x32_bf16 v[86:89], v[178:181], v[210:213], v[86:89]
	v_mfma_f32_16x16x32_bf16 v[82:85], v[186:189], v[210:213], v[82:85]
	v_mfma_f32_16x16x32_bf16 v[70:73], v[178:181], v[218:221], v[70:73]
	v_mfma_f32_16x16x32_bf16 v[66:69], v[186:189], v[218:221], v[66:69]
	v_mfma_f32_16x16x32_bf16 v[118:121], v[182:185], v[198:201], v[118:121]
	v_mfma_f32_16x16x32_bf16 v[114:117], v[190:193], v[198:201], v[114:117]
	v_mfma_f32_16x16x32_bf16 v[102:105], v[182:185], v[206:209], v[102:105]
	v_mfma_f32_16x16x32_bf16 v[98:101], v[190:193], v[206:209], v[98:101]
	v_mfma_f32_16x16x32_bf16 v[86:89], v[182:185], v[214:217], v[86:89]
	v_mfma_f32_16x16x32_bf16 v[82:85], v[190:193], v[214:217], v[82:85]
	v_mfma_f32_16x16x32_bf16 v[70:73], v[182:185], v[222:225], v[70:73]
	v_mfma_f32_16x16x32_bf16 v[66:69], v[190:193], v[222:225], v[66:69]
	s_setprio 0
	s_barrier
	s_add_i32 s46, s70, s52
	v_lshl_add_u64 v[226:227], v[226:227], 0, s[12:13]
	s_mov_b32 m0, s46
	ds_read_b128 v[194:197], v160 offset:49152
	ds_read_b128 v[198:201], v160 offset:50176
	ds_read_b128 v[202:205], v160 offset:51200
	ds_read_b128 v[206:209], v160 offset:52224
	ds_read_b128 v[210:213], v160 offset:53248
	ds_read_b128 v[214:217], v160 offset:54272
	ds_read_b128 v[218:221], v160 offset:55296
	ds_read_b128 v[222:225], v160 offset:56320
	global_load_lds_dwordx4 v[226:227], off
	s_add_i32 m0, s46, 0x2000
	s_add_u32 s44, s44, 0x100080
	v_lshl_add_u64 v[226:227], v[228:229], 0, s[12:13]
	s_addc_u32 s45, s45, 0
	s_add_i32 s46, s71, s52
	global_load_lds_dwordx4 v[226:227], off
	v_lshl_add_u64 v[226:227], s[44:45], 0, v[132:133]
	s_mov_b32 m0, s46
	s_nop 0
	global_load_lds_dwordx4 v[226:227], off
	v_lshl_add_u64 v[226:227], s[44:45], 0, v[136:137]
	s_add_i32 m0, s46, 0x2000
	s_nop 0
	global_load_lds_dwordx4 v[226:227], off
	v_lshl_add_u64 v[226:227], v[230:231], 0, s[12:13]
	s_mov_b32 m0, s60
	s_nop 0
	global_load_lds_dwordx4 v[226:227], off
	v_lshl_add_u64 v[226:227], v[232:233], 0, s[12:13]
	s_mov_b32 m0, s61
	s_nop 0
	global_load_lds_dwordx4 v[226:227], off
	s_waitcnt vmcnt(8)
	s_waitcnt lgkmcnt(0)
	s_barrier
	s_setprio 1
	s_waitcnt lgkmcnt(0)
	v_mfma_f32_16x16x32_bf16 v[62:65], v[162:165], v[194:197], v[62:65]
	v_mfma_f32_16x16x32_bf16 v[58:61], v[170:173], v[194:197], v[58:61]
	v_mfma_f32_16x16x32_bf16 v[46:49], v[162:165], v[202:205], v[46:49]
	v_mfma_f32_16x16x32_bf16 v[42:45], v[170:173], v[202:205], v[42:45]
	v_mfma_f32_16x16x32_bf16 v[30:33], v[162:165], v[210:213], v[30:33]
	v_mfma_f32_16x16x32_bf16 v[26:29], v[170:173], v[210:213], v[26:29]
	v_mfma_f32_16x16x32_bf16 v[14:17], v[162:165], v[218:221], v[14:17]
	v_mfma_f32_16x16x32_bf16 v[10:13], v[170:173], v[218:221], v[10:13]
	v_mfma_f32_16x16x32_bf16 v[62:65], v[166:169], v[198:201], v[62:65]
	v_mfma_f32_16x16x32_bf16 v[58:61], v[174:177], v[198:201], v[58:61]
	v_mfma_f32_16x16x32_bf16 v[46:49], v[166:169], v[206:209], v[46:49]
	v_mfma_f32_16x16x32_bf16 v[42:45], v[174:177], v[206:209], v[42:45]
	v_mfma_f32_16x16x32_bf16 v[30:33], v[166:169], v[214:217], v[30:33]
	v_mfma_f32_16x16x32_bf16 v[26:29], v[174:177], v[214:217], v[26:29]
	v_mfma_f32_16x16x32_bf16 v[14:17], v[166:169], v[222:225], v[14:17]
	v_mfma_f32_16x16x32_bf16 v[10:13], v[174:177], v[222:225], v[10:13]
	s_setprio 0
	s_setprio 1
	v_mfma_f32_16x16x32_bf16 v[54:57], v[178:181], v[194:197], v[54:57]
	v_mfma_f32_16x16x32_bf16 v[50:53], v[186:189], v[194:197], v[50:53]
	v_mfma_f32_16x16x32_bf16 v[38:41], v[178:181], v[202:205], v[38:41]
	v_mfma_f32_16x16x32_bf16 v[34:37], v[186:189], v[202:205], v[34:37]
	v_mfma_f32_16x16x32_bf16 v[22:25], v[178:181], v[210:213], v[22:25]
	v_mfma_f32_16x16x32_bf16 v[18:21], v[186:189], v[210:213], v[18:21]
	v_mfma_f32_16x16x32_bf16 v[6:9], v[178:181], v[218:221], v[6:9]
	v_mfma_f32_16x16x32_bf16 v[2:5], v[186:189], v[218:221], v[2:5]
	v_mfma_f32_16x16x32_bf16 v[54:57], v[182:185], v[198:201], v[54:57]
	v_mfma_f32_16x16x32_bf16 v[50:53], v[190:193], v[198:201], v[50:53]
	v_mfma_f32_16x16x32_bf16 v[38:41], v[182:185], v[206:209], v[38:41]
	v_mfma_f32_16x16x32_bf16 v[34:37], v[190:193], v[206:209], v[34:37]
	v_mfma_f32_16x16x32_bf16 v[22:25], v[182:185], v[214:217], v[22:25]
	v_mfma_f32_16x16x32_bf16 v[18:21], v[190:193], v[214:217], v[18:21]
	v_mfma_f32_16x16x32_bf16 v[6:9], v[182:185], v[222:225], v[6:9]
	v_mfma_f32_16x16x32_bf16 v[2:5], v[190:193], v[222:225], v[2:5]
	s_setprio 0
	s_barrier
	s_add_i32 s69, s69, 2
	s_add_u32 s42, s42, 0x100
	s_addc_u32 s43, s43, 0
	s_cmp_gt_u32 s69, 61
	s_cbranch_scc0 .LBB0_454
	s_and_b64 vcc, exec, s[14:15]
	s_cbranch_vccz .LBB0_457
	s_barrier

.LBB0_544:
	s_add_u32 s20, s44, s18
	s_addc_u32 s21, s45, s19
	s_add_u32 s20, s20, 0xa300100
	s_addc_u32 s21, s21, 0
	s_add_u32 s51, s48, s18
	s_addc_u32 s52, s49, s19
	s_cmpk_eq_i32 s18, 0x1f00
	s_cselect_b32 s23, s17, s21
	s_cselect_b32 s22, s16, s20
	v_add_u32_e32 v155, s93, v153
	s_cselect_b32 s21, s7, s52
	s_cselect_b32 s20, s6, s51
	s_add_i32 s51, 0, 0x14000
	ds_read_b128 v[156:159], v155
	ds_read_b128 v[160:163], v155 offset:1024
	ds_read_b128 v[164:167], v155 offset:2048
	ds_read_b128 v[168:171], v155 offset:3072
	v_add_u32_e32 v155, s51, v153
	ds_read_b128 v[172:175], v155
	ds_read_b128 v[176:179], v155 offset:1024
	ds_read_b128 v[180:183], v155 offset:2048
	ds_read_b128 v[184:187], v155 offset:3072
	v_lshl_add_u64 v[220:221], v[144:145], 0, s[18:19]
	s_add_i32 m0, s14, 0xc000
	ds_read_b128 v[188:191], v154
	ds_read_b128 v[192:195], v154 offset:1024
	ds_read_b128 v[196:199], v154 offset:2048
	ds_read_b128 v[200:203], v154 offset:3072
	ds_read_b128 v[204:207], v154 offset:4096
	ds_read_b128 v[208:211], v154 offset:5120
	ds_read_b128 v[212:215], v154 offset:6144
	ds_read_b128 v[216:219], v154 offset:7168
	global_load_lds_dwordx4 v[220:221], off
	v_lshl_add_u64 v[220:221], v[146:147], 0, s[18:19]
	s_add_i32 m0, s14, 0xe000
	s_nop 0
	global_load_lds_dwordx4 v[220:221], off
	s_cmp_lg_u32 s10, 0
	s_cbranch_scc1 .Lpg8r4
	s_waitcnt vmcnt(8)
	s_branch .Lpg8e4

.Lpg8e4:
	s_waitcnt lgkmcnt(0)
	s_barrier
	s_setprio 1
	s_waitcnt lgkmcnt(0)
	v_mfma_f32_16x16x32_bf16 v[126:129], v[156:159], v[188:191], v[126:129]
	v_mfma_f32_16x16x32_bf16 v[122:125], v[164:167], v[188:191], v[122:125]
	v_mfma_f32_16x16x32_bf16 v[110:113], v[156:159], v[196:199], v[110:113]
	v_mfma_f32_16x16x32_bf16 v[106:109], v[164:167], v[196:199], v[106:109]
	v_mfma_f32_16x16x32_bf16 v[94:97], v[156:159], v[204:207], v[94:97]
	v_mfma_f32_16x16x32_bf16 v[90:93], v[164:167], v[204:207], v[90:93]
	v_mfma_f32_16x16x32_bf16 v[78:81], v[156:159], v[212:215], v[78:81]
	v_mfma_f32_16x16x32_bf16 v[74:77], v[164:167], v[212:215], v[74:77]
	v_mfma_f32_16x16x32_bf16 v[126:129], v[160:163], v[192:195], v[126:129]
	v_mfma_f32_16x16x32_bf16 v[122:125], v[168:171], v[192:195], v[122:125]
	v_mfma_f32_16x16x32_bf16 v[110:113], v[160:163], v[200:203], v[110:113]
	v_mfma_f32_16x16x32_bf16 v[106:109], v[168:171], v[200:203], v[106:109]
	v_mfma_f32_16x16x32_bf16 v[94:97], v[160:163], v[208:211], v[94:97]
	v_mfma_f32_16x16x32_bf16 v[90:93], v[168:171], v[208:211], v[90:93]
	v_mfma_f32_16x16x32_bf16 v[78:81], v[160:163], v[216:219], v[78:81]
	v_mfma_f32_16x16x32_bf16 v[74:77], v[168:171], v[216:219], v[74:77]
	s_setprio 0
	s_setprio 1
	v_mfma_f32_16x16x32_bf16 v[118:121], v[172:175], v[188:191], v[118:121]
	v_mfma_f32_16x16x32_bf16 v[114:117], v[180:183], v[188:191], v[114:117]
	v_mfma_f32_16x16x32_bf16 v[102:105], v[172:175], v[196:199], v[102:105]
	v_mfma_f32_16x16x32_bf16 v[98:101], v[180:183], v[196:199], v[98:101]
	v_mfma_f32_16x16x32_bf16 v[86:89], v[172:175], v[204:207], v[86:89]
	v_mfma_f32_16x16x32_bf16 v[82:85], v[180:183], v[204:207], v[82:85]
	v_mfma_f32_16x16x32_bf16 v[70:73], v[172:175], v[212:215], v[70:73]
	v_mfma_f32_16x16x32_bf16 v[66:69], v[180:183], v[212:215], v[66:69]
	v_mfma_f32_16x16x32_bf16 v[118:121], v[176:179], v[192:195], v[118:121]
	v_mfma_f32_16x16x32_bf16 v[114:117], v[184:187], v[192:195], v[114:117]
	v_mfma_f32_16x16x32_bf16 v[102:105], v[176:179], v[200:203], v[102:105]
	v_mfma_f32_16x16x32_bf16 v[98:101], v[184:187], v[200:203], v[98:101]
	v_mfma_f32_16x16x32_bf16 v[86:89], v[176:179], v[208:211], v[86:89]
	v_mfma_f32_16x16x32_bf16 v[82:85], v[184:187], v[208:211], v[82:85]
	v_mfma_f32_16x16x32_bf16 v[70:73], v[176:179], v[216:219], v[70:73]
	v_mfma_f32_16x16x32_bf16 v[66:69], v[184:187], v[216:219], v[66:69]
	s_setprio 0
	s_barrier
	s_add_i32 s52, s93, s37
	v_lshl_add_u64 v[220:221], s[20:21], 0, v[136:137]
	s_mov_b32 m0, s52
	ds_read_b128 v[188:191], v154 offset:16384
	ds_read_b128 v[192:195], v154 offset:17408
	ds_read_b128 v[196:199], v154 offset:18432
	ds_read_b128 v[200:203], v154 offset:19456
	ds_read_b128 v[204:207], v154 offset:20480
	ds_read_b128 v[208:211], v154 offset:21504
	ds_read_b128 v[212:215], v154 offset:22528
	ds_read_b128 v[216:219], v154 offset:23552
	global_load_lds_dwordx4 v[220:221], off
	s_add_i32 m0, s52, 0x2000
	s_add_u32 s52, s20, 0x100000
	v_lshl_add_u64 v[222:223], s[20:21], 0, v[142:143]
	s_addc_u32 s53, s21, 0
	s_add_i32 s51, s51, s37
	global_load_lds_dwordx4 v[222:223], off
	v_lshl_add_u64 v[224:225], s[52:53], 0, v[136:137]
	s_mov_b32 m0, s51
	v_lshl_add_u64 v[226:227], s[22:23], 0, v[140:141]
	global_load_lds_dwordx4 v[224:225], off
	v_lshl_add_u64 v[224:225], s[52:53], 0, v[142:143]
	s_add_i32 m0, s51, 0x2000
	s_nop 0
	global_load_lds_dwordx4 v[224:225], off
	v_lshl_add_u64 v[224:225], s[22:23], 0, v[138:139]
	s_mov_b32 m0, s14
	s_nop 0
	global_load_lds_dwordx4 v[224:225], off
	s_mov_b32 m0, s38
	s_nop 0
	global_load_lds_dwordx4 v[226:227], off
	s_cmp_lg_u32 s10, 0
	s_cbranch_scc1 .Lpg8r5
	s_waitcnt vmcnt(8)
	s_branch .Lpg8e5

.Lpg8e5:
	s_waitcnt lgkmcnt(0)
	s_barrier
	s_setprio 1
	s_waitcnt lgkmcnt(0)
	v_mfma_f32_16x16x32_bf16 v[62:65], v[156:159], v[188:191], v[62:65]
	v_mfma_f32_16x16x32_bf16 v[58:61], v[164:167], v[188:191], v[58:61]
	v_mfma_f32_16x16x32_bf16 v[46:49], v[156:159], v[196:199], v[46:49]
	v_mfma_f32_16x16x32_bf16 v[42:45], v[164:167], v[196:199], v[42:45]
	v_mfma_f32_16x16x32_bf16 v[30:33], v[156:159], v[204:207], v[30:33]
	v_mfma_f32_16x16x32_bf16 v[26:29], v[164:167], v[204:207], v[26:29]
	v_mfma_f32_16x16x32_bf16 v[14:17], v[156:159], v[212:215], v[14:17]
	v_mfma_f32_16x16x32_bf16 v[10:13], v[164:167], v[212:215], v[10:13]
	v_mfma_f32_16x16x32_bf16 v[62:65], v[160:163], v[192:195], v[62:65]
	v_mfma_f32_16x16x32_bf16 v[58:61], v[168:171], v[192:195], v[58:61]
	v_mfma_f32_16x16x32_bf16 v[46:49], v[160:163], v[200:203], v[46:49]
	v_mfma_f32_16x16x32_bf16 v[42:45], v[168:171], v[200:203], v[42:45]
	v_mfma_f32_16x16x32_bf16 v[30:33], v[160:163], v[208:211], v[30:33]
	v_mfma_f32_16x16x32_bf16 v[26:29], v[168:171], v[208:211], v[26:29]
	v_mfma_f32_16x16x32_bf16 v[14:17], v[160:163], v[216:219], v[14:17]
	v_mfma_f32_16x16x32_bf16 v[10:13], v[168:171], v[216:219], v[10:13]
	s_setprio 0
	s_setprio 1
	v_mfma_f32_16x16x32_bf16 v[54:57], v[172:175], v[188:191], v[54:57]
	v_mfma_f32_16x16x32_bf16 v[50:53], v[180:183], v[188:191], v[50:53]
	v_mfma_f32_16x16x32_bf16 v[38:41], v[172:175], v[196:199], v[38:41]
	v_mfma_f32_16x16x32_bf16 v[34:37], v[180:183], v[196:199], v[34:37]
	v_mfma_f32_16x16x32_bf16 v[22:25], v[172:175], v[204:207], v[22:25]
	v_mfma_f32_16x16x32_bf16 v[18:21], v[180:183], v[204:207], v[18:21]
	v_mfma_f32_16x16x32_bf16 v[6:9], v[172:175], v[212:215], v[6:9]
	v_mfma_f32_16x16x32_bf16 v[2:5], v[180:183], v[212:215], v[2:5]
	v_mfma_f32_16x16x32_bf16 v[54:57], v[176:179], v[192:195], v[54:57]
	v_mfma_f32_16x16x32_bf16 v[50:53], v[184:187], v[192:195], v[50:53]
	v_mfma_f32_16x16x32_bf16 v[38:41], v[176:179], v[200:203], v[38:41]
	v_mfma_f32_16x16x32_bf16 v[34:37], v[184:187], v[200:203], v[34:37]
	v_mfma_f32_16x16x32_bf16 v[22:25], v[176:179], v[208:211], v[22:25]
	v_mfma_f32_16x16x32_bf16 v[18:21], v[184:187], v[208:211], v[18:21]
	v_mfma_f32_16x16x32_bf16 v[6:9], v[176:179], v[216:219], v[6:9]
	v_mfma_f32_16x16x32_bf16 v[2:5], v[184:187], v[216:219], v[2:5]
	s_setprio 0
	s_barrier
	s_add_i32 s51, 0, 0x18000
	v_add_u32_e32 v155, s51, v153
	s_add_i32 s52, 0, 0x1c000
	ds_read_b128 v[156:159], v155
	ds_read_b128 v[160:163], v155 offset:1024
	ds_read_b128 v[164:167], v155 offset:2048
	ds_read_b128 v[168:171], v155 offset:3072
	v_add_u32_e32 v155, s52, v153
	ds_read_b128 v[172:175], v155
	ds_read_b128 v[176:179], v155 offset:1024
	ds_read_b128 v[180:183], v155 offset:2048
	ds_read_b128 v[184:187], v155 offset:3072
	s_add_u32 s22, s22, 0x100000
	s_addc_u32 s23, s23, 0
	s_mov_b32 m0, s39
	v_lshl_add_u64 v[228:229], s[22:23], 0, v[138:139]
	ds_read_b128 v[188:191], v154 offset:32768
	ds_read_b128 v[192:195], v154 offset:33792
	ds_read_b128 v[196:199], v154 offset:34816
	ds_read_b128 v[200:203], v154 offset:35840
	ds_read_b128 v[204:207], v154 offset:36864
	ds_read_b128 v[208:211], v154 offset:37888
	ds_read_b128 v[212:215], v154 offset:38912
	ds_read_b128 v[216:219], v154 offset:39936
	global_load_lds_dwordx4 v[228:229], off
	v_lshl_add_u64 v[228:229], s[22:23], 0, v[140:141]
	s_mov_b32 m0, s40
	s_nop 0
	global_load_lds_dwordx4 v[228:229], off
	s_waitcnt vmcnt(8)
	s_waitcnt lgkmcnt(0)
	s_barrier
	s_setprio 1
	s_waitcnt lgkmcnt(0)
	v_mfma_f32_16x16x32_bf16 v[126:129], v[156:159], v[188:191], v[126:129]
	v_mfma_f32_16x16x32_bf16 v[122:125], v[164:167], v[188:191], v[122:125]
	v_mfma_f32_16x16x32_bf16 v[110:113], v[156:159], v[196:199], v[110:113]
	v_mfma_f32_16x16x32_bf16 v[106:109], v[164:167], v[196:199], v[106:109]
	v_mfma_f32_16x16x32_bf16 v[94:97], v[156:159], v[204:207], v[94:97]
	v_mfma_f32_16x16x32_bf16 v[90:93], v[164:167], v[204:207], v[90:93]
	v_mfma_f32_16x16x32_bf16 v[78:81], v[156:159], v[212:215], v[78:81]
	v_mfma_f32_16x16x32_bf16 v[74:77], v[164:167], v[212:215], v[74:77]
	v_mfma_f32_16x16x32_bf16 v[126:129], v[160:163], v[192:195], v[126:129]
	v_mfma_f32_16x16x32_bf16 v[122:125], v[168:171], v[192:195], v[122:125]
	v_mfma_f32_16x16x32_bf16 v[110:113], v[160:163], v[200:203], v[110:113]
	v_mfma_f32_16x16x32_bf16 v[106:109], v[168:171], v[200:203], v[106:109]
	v_mfma_f32_16x16x32_bf16 v[94:97], v[160:163], v[208:211], v[94:97]
	v_mfma_f32_16x16x32_bf16 v[90:93], v[168:171], v[208:211], v[90:93]
	v_mfma_f32_16x16x32_bf16 v[78:81], v[160:163], v[216:219], v[78:81]
	v_mfma_f32_16x16x32_bf16 v[74:77], v[168:171], v[216:219], v[74:77]
	s_setprio 0
	s_setprio 1
	v_mfma_f32_16x16x32_bf16 v[118:121], v[172:175], v[188:191], v[118:121]
	v_mfma_f32_16x16x32_bf16 v[114:117], v[180:183], v[188:191], v[114:117]
	v_mfma_f32_16x16x32_bf16 v[102:105], v[172:175], v[196:199], v[102:105]
	v_mfma_f32_16x16x32_bf16 v[98:101], v[180:183], v[196:199], v[98:101]
	v_mfma_f32_16x16x32_bf16 v[86:89], v[172:175], v[204:207], v[86:89]
	v_mfma_f32_16x16x32_bf16 v[82:85], v[180:183], v[204:207], v[82:85]
	v_mfma_f32_16x16x32_bf16 v[70:73], v[172:175], v[212:215], v[70:73]
	v_mfma_f32_16x16x32_bf16 v[66:69], v[180:183], v[212:215], v[66:69]
	v_mfma_f32_16x16x32_bf16 v[118:121], v[176:179], v[192:195], v[118:121]
	v_mfma_f32_16x16x32_bf16 v[114:117], v[184:187], v[192:195], v[114:117]
	v_mfma_f32_16x16x32_bf16 v[102:105], v[176:179], v[200:203], v[102:105]
	v_mfma_f32_16x16x32_bf16 v[98:101], v[184:187], v[200:203], v[98:101]
	v_mfma_f32_16x16x32_bf16 v[86:89], v[176:179], v[208:211], v[86:89]
	v_mfma_f32_16x16x32_bf16 v[82:85], v[184:187], v[208:211], v[82:85]
	v_mfma_f32_16x16x32_bf16 v[70:73], v[176:179], v[216:219], v[70:73]
	v_mfma_f32_16x16x32_bf16 v[66:69], v[184:187], v[216:219], v[66:69]
	s_setprio 0
	s_barrier
	s_add_i32 s22, s51, s37
	v_lshl_add_u64 v[220:221], v[220:221], 0, s[12:13]
	s_mov_b32 m0, s22
	ds_read_b128 v[188:191], v154 offset:49152
	ds_read_b128 v[192:195], v154 offset:50176
	ds_read_b128 v[196:199], v154 offset:51200
	ds_read_b128 v[200:203], v154 offset:52224
	ds_read_b128 v[204:207], v154 offset:53248
	ds_read_b128 v[208:211], v154 offset:54272
	ds_read_b128 v[212:215], v154 offset:55296
	ds_read_b128 v[216:219], v154 offset:56320
	global_load_lds_dwordx4 v[220:221], off
	s_add_i32 m0, s22, 0x2000
	s_add_u32 s20, s20, 0x100080
	v_lshl_add_u64 v[220:221], v[222:223], 0, s[12:13]
	s_addc_u32 s21, s21, 0
	s_add_i32 s22, s52, s37
	global_load_lds_dwordx4 v[220:221], off
	v_lshl_add_u64 v[220:221], s[20:21], 0, v[136:137]
	s_mov_b32 m0, s22
	s_nop 0
	global_load_lds_dwordx4 v[220:221], off
	v_lshl_add_u64 v[220:221], s[20:21], 0, v[142:143]
	s_add_i32 m0, s22, 0x2000
	s_nop 0
	global_load_lds_dwordx4 v[220:221], off
	v_lshl_add_u64 v[220:221], v[224:225], 0, s[12:13]
	s_mov_b32 m0, s42
	s_nop 0
	global_load_lds_dwordx4 v[220:221], off
	v_lshl_add_u64 v[220:221], v[226:227], 0, s[12:13]
	s_mov_b32 m0, s43
	s_nop 0
	global_load_lds_dwordx4 v[220:221], off
	s_waitcnt vmcnt(8)
	s_waitcnt lgkmcnt(0)
	s_barrier
	s_setprio 1
	s_waitcnt lgkmcnt(0)
	v_mfma_f32_16x16x32_bf16 v[62:65], v[156:159], v[188:191], v[62:65]
	v_mfma_f32_16x16x32_bf16 v[58:61], v[164:167], v[188:191], v[58:61]
	v_mfma_f32_16x16x32_bf16 v[46:49], v[156:159], v[196:199], v[46:49]
	v_mfma_f32_16x16x32_bf16 v[42:45], v[164:167], v[196:199], v[42:45]
	v_mfma_f32_16x16x32_bf16 v[30:33], v[156:159], v[204:207], v[30:33]
	v_mfma_f32_16x16x32_bf16 v[26:29], v[164:167], v[204:207], v[26:29]
	v_mfma_f32_16x16x32_bf16 v[14:17], v[156:159], v[212:215], v[14:17]
	v_mfma_f32_16x16x32_bf16 v[10:13], v[164:167], v[212:215], v[10:13]
	v_mfma_f32_16x16x32_bf16 v[62:65], v[160:163], v[192:195], v[62:65]
	v_mfma_f32_16x16x32_bf16 v[58:61], v[168:171], v[192:195], v[58:61]
	v_mfma_f32_16x16x32_bf16 v[46:49], v[160:163], v[200:203], v[46:49]
	v_mfma_f32_16x16x32_bf16 v[42:45], v[168:171], v[200:203], v[42:45]
	v_mfma_f32_16x16x32_bf16 v[30:33], v[160:163], v[208:211], v[30:33]
	v_mfma_f32_16x16x32_bf16 v[26:29], v[168:171], v[208:211], v[26:29]
	v_mfma_f32_16x16x32_bf16 v[14:17], v[160:163], v[216:219], v[14:17]
	v_mfma_f32_16x16x32_bf16 v[10:13], v[168:171], v[216:219], v[10:13]
	s_setprio 0
	s_setprio 1
	v_mfma_f32_16x16x32_bf16 v[54:57], v[172:175], v[188:191], v[54:57]
	v_mfma_f32_16x16x32_bf16 v[50:53], v[180:183], v[188:191], v[50:53]
	v_mfma_f32_16x16x32_bf16 v[38:41], v[172:175], v[196:199], v[38:41]
	v_mfma_f32_16x16x32_bf16 v[34:37], v[180:183], v[196:199], v[34:37]
	v_mfma_f32_16x16x32_bf16 v[22:25], v[172:175], v[204:207], v[22:25]
	v_mfma_f32_16x16x32_bf16 v[18:21], v[180:183], v[204:207], v[18:21]
	v_mfma_f32_16x16x32_bf16 v[6:9], v[172:175], v[212:215], v[6:9]
	v_mfma_f32_16x16x32_bf16 v[2:5], v[180:183], v[212:215], v[2:5]
	v_mfma_f32_16x16x32_bf16 v[54:57], v[176:179], v[192:195], v[54:57]
	v_mfma_f32_16x16x32_bf16 v[50:53], v[184:187], v[192:195], v[50:53]
	v_mfma_f32_16x16x32_bf16 v[38:41], v[176:179], v[200:203], v[38:41]
	v_mfma_f32_16x16x32_bf16 v[34:37], v[184:187], v[200:203], v[34:37]
	v_mfma_f32_16x16x32_bf16 v[22:25], v[176:179], v[208:211], v[22:25]
	v_mfma_f32_16x16x32_bf16 v[18:21], v[184:187], v[208:211], v[18:21]
	v_mfma_f32_16x16x32_bf16 v[6:9], v[176:179], v[216:219], v[6:9]
	v_mfma_f32_16x16x32_bf16 v[2:5], v[184:187], v[216:219], v[2:5]
	s_setprio 0
	s_barrier
	s_add_i32 s50, s50, 2
	s_add_u32 s18, s18, 0x100
	s_addc_u32 s19, s19, 0
	s_cmp_gt_u32 s50, 61
	s_cbranch_scc0 .LBB0_544
	s_cmpk_lt_u32 s36, 0x100
	s_cbranch_scc0 .LBB0_530
	s_barrier
	s_branch .LBB0_530

.LBB0_564:
	ds_read_b128 v[152:155], v149
	ds_read_b128 v[156:159], v149 offset:1024
	ds_read_b128 v[160:163], v149 offset:2048
	ds_read_b128 v[164:167], v149 offset:3072
	ds_read_b128 v[168:171], v150
	ds_read_b128 v[172:175], v150 offset:1024
	ds_read_b128 v[176:179], v150 offset:2048
	ds_read_b128 v[180:183], v150 offset:3072
	s_add_u32 s40, s34, s38
	s_addc_u32 s41, s35, s39
	s_add_u32 s42, s40, 0x100
	s_addc_u32 s43, s41, 0
	s_add_u32 s72, s69, s38
	s_addc_u32 s73, s70, s39
	s_cmp_eq_u32 s38, 0
	s_cselect_b64 s[40:41], -1, 0
	s_and_b64 s[40:41], s[36:37], s[40:41]
	s_cmpk_eq_i32 s38, 0x1f00
	v_cndmask_b32_e64 v184, 0, 1, s[40:41]
	s_cselect_b32 s43, s25, s43
	s_cselect_b32 s42, s67, s42
	v_readfirstlane_b32 s74, v184
	s_cselect_b32 s41, s23, s73
	s_cselect_b32 s40, s68, s72
	v_lshl_add_u64 v[216:217], v[142:143], 0, s[38:39]
	s_add_i32 m0, s31, 0xc000
	ds_read_b128 v[184:187], v151
	ds_read_b128 v[188:191], v151 offset:1024
	ds_read_b128 v[192:195], v151 offset:2048
	ds_read_b128 v[196:199], v151 offset:3072
	ds_read_b128 v[200:203], v151 offset:4096
	ds_read_b128 v[204:207], v151 offset:5120
	ds_read_b128 v[208:211], v151 offset:6144
	ds_read_b128 v[212:215], v151 offset:7168
	global_load_lds_dwordx4 v[216:217], off
	v_lshl_add_u64 v[216:217], v[144:145], 0, s[38:39]
	s_add_i32 m0, s31, 0xe000
	s_and_b32 s74, s74, 1
	global_load_lds_dwordx4 v[216:217], off
	s_cmp_lg_u32 s74, 0
	s_cbranch_scc1 .Lpg8r6
	s_waitcnt vmcnt(8)
	s_branch .Lpg8e6

.Lpg8e6:
	s_waitcnt lgkmcnt(0)
	s_barrier
	s_setprio 1
	s_waitcnt lgkmcnt(0)
	v_mfma_f32_16x16x32_bf16 v[126:129], v[152:155], v[184:187], v[126:129]
	v_mfma_f32_16x16x32_bf16 v[122:125], v[160:163], v[184:187], v[122:125]
	v_mfma_f32_16x16x32_bf16 v[114:117], v[152:155], v[192:195], v[114:117]
	v_mfma_f32_16x16x32_bf16 v[106:109], v[160:163], v[192:195], v[106:109]
	v_mfma_f32_16x16x32_bf16 v[98:101], v[152:155], v[200:203], v[98:101]
	v_mfma_f32_16x16x32_bf16 v[90:93], v[160:163], v[200:203], v[90:93]
	v_mfma_f32_16x16x32_bf16 v[82:85], v[152:155], v[208:211], v[82:85]
	v_mfma_f32_16x16x32_bf16 v[74:77], v[160:163], v[208:211], v[74:77]
	v_mfma_f32_16x16x32_bf16 v[126:129], v[156:159], v[188:191], v[126:129]
	v_mfma_f32_16x16x32_bf16 v[122:125], v[164:167], v[188:191], v[122:125]
	v_mfma_f32_16x16x32_bf16 v[114:117], v[156:159], v[196:199], v[114:117]
	v_mfma_f32_16x16x32_bf16 v[106:109], v[164:167], v[196:199], v[106:109]
	v_mfma_f32_16x16x32_bf16 v[98:101], v[156:159], v[204:207], v[98:101]
	v_mfma_f32_16x16x32_bf16 v[90:93], v[164:167], v[204:207], v[90:93]
	v_mfma_f32_16x16x32_bf16 v[82:85], v[156:159], v[212:215], v[82:85]
	v_mfma_f32_16x16x32_bf16 v[74:77], v[164:167], v[212:215], v[74:77]
	s_setprio 0
	s_setprio 1
	v_mfma_f32_16x16x32_bf16 v[118:121], v[168:171], v[184:187], v[118:121]
	v_mfma_f32_16x16x32_bf16 v[110:113], v[176:179], v[184:187], v[110:113]
	v_mfma_f32_16x16x32_bf16 v[102:105], v[168:171], v[192:195], v[102:105]
	v_mfma_f32_16x16x32_bf16 v[94:97], v[176:179], v[192:195], v[94:97]
	v_mfma_f32_16x16x32_bf16 v[86:89], v[168:171], v[200:203], v[86:89]
	v_mfma_f32_16x16x32_bf16 v[78:81], v[176:179], v[200:203], v[78:81]
	v_mfma_f32_16x16x32_bf16 v[70:73], v[168:171], v[208:211], v[70:73]
	v_mfma_f32_16x16x32_bf16 v[66:69], v[176:179], v[208:211], v[66:69]
	v_mfma_f32_16x16x32_bf16 v[118:121], v[172:175], v[188:191], v[118:121]
	v_mfma_f32_16x16x32_bf16 v[110:113], v[180:183], v[188:191], v[110:113]
	v_mfma_f32_16x16x32_bf16 v[102:105], v[172:175], v[196:199], v[102:105]
	v_mfma_f32_16x16x32_bf16 v[94:97], v[180:183], v[196:199], v[94:97]
	v_mfma_f32_16x16x32_bf16 v[86:89], v[172:175], v[204:207], v[86:89]
	v_mfma_f32_16x16x32_bf16 v[78:81], v[180:183], v[204:207], v[78:81]
	v_mfma_f32_16x16x32_bf16 v[70:73], v[172:175], v[212:215], v[70:73]
	v_mfma_f32_16x16x32_bf16 v[66:69], v[180:183], v[212:215], v[66:69]
	s_setprio 0
	s_barrier
	s_add_i32 s72, s93, s54
	v_lshl_add_u64 v[216:217], s[40:41], 0, v[132:133]
	s_mov_b32 m0, s72
	ds_read_b128 v[184:187], v151 offset:16384
	ds_read_b128 v[188:191], v151 offset:17408
	ds_read_b128 v[192:195], v151 offset:18432
	ds_read_b128 v[196:199], v151 offset:19456
	ds_read_b128 v[200:203], v151 offset:20480
	ds_read_b128 v[204:207], v151 offset:21504
	ds_read_b128 v[208:211], v151 offset:22528
	ds_read_b128 v[212:215], v151 offset:23552
	global_load_lds_dwordx4 v[216:217], off
	s_add_i32 m0, s72, 0x2000
	s_add_u32 s72, s40, 0x100000
	v_lshl_add_u64 v[218:219], s[40:41], 0, v[136:137]
	s_addc_u32 s73, s41, 0
	s_add_i32 s75, s60, s54
	global_load_lds_dwordx4 v[218:219], off
	v_lshl_add_u64 v[220:221], s[72:73], 0, v[132:133]
	s_mov_b32 m0, s75
	v_lshl_add_u64 v[222:223], s[42:43], 0, v[134:135]
	global_load_lds_dwordx4 v[220:221], off
	v_lshl_add_u64 v[220:221], s[72:73], 0, v[136:137]
	s_add_i32 m0, s75, 0x2000
	s_nop 0
	global_load_lds_dwordx4 v[220:221], off
	v_lshl_add_u64 v[220:221], s[42:43], 0, v[130:131]
	s_mov_b32 m0, s31
	s_nop 0
	global_load_lds_dwordx4 v[220:221], off
	s_mov_b32 m0, s55
	s_nop 0
	global_load_lds_dwordx4 v[222:223], off
	s_cmp_lg_u32 s74, 0
	s_cbranch_scc1 .Lpg8r7
	s_waitcnt vmcnt(8)
	s_branch .Lpg8e7

.Lpg8e7:
	s_waitcnt lgkmcnt(0)
	s_barrier
	s_setprio 1
	s_waitcnt lgkmcnt(0)
	v_mfma_f32_16x16x32_bf16 v[62:65], v[152:155], v[184:187], v[62:65]
	v_mfma_f32_16x16x32_bf16 v[58:61], v[160:163], v[184:187], v[58:61]
	v_mfma_f32_16x16x32_bf16 v[50:53], v[152:155], v[192:195], v[50:53]
	v_mfma_f32_16x16x32_bf16 v[42:45], v[160:163], v[192:195], v[42:45]
	v_mfma_f32_16x16x32_bf16 v[34:37], v[152:155], v[200:203], v[34:37]
	v_mfma_f32_16x16x32_bf16 v[26:29], v[160:163], v[200:203], v[26:29]
	v_mfma_f32_16x16x32_bf16 v[18:21], v[152:155], v[208:211], v[18:21]
	v_mfma_f32_16x16x32_bf16 v[10:13], v[160:163], v[208:211], v[10:13]
	v_mfma_f32_16x16x32_bf16 v[62:65], v[156:159], v[188:191], v[62:65]
	v_mfma_f32_16x16x32_bf16 v[58:61], v[164:167], v[188:191], v[58:61]
	v_mfma_f32_16x16x32_bf16 v[50:53], v[156:159], v[196:199], v[50:53]
	v_mfma_f32_16x16x32_bf16 v[42:45], v[164:167], v[196:199], v[42:45]
	v_mfma_f32_16x16x32_bf16 v[34:37], v[156:159], v[204:207], v[34:37]
	v_mfma_f32_16x16x32_bf16 v[26:29], v[164:167], v[204:207], v[26:29]
	v_mfma_f32_16x16x32_bf16 v[18:21], v[156:159], v[212:215], v[18:21]
	v_mfma_f32_16x16x32_bf16 v[10:13], v[164:167], v[212:215], v[10:13]
	s_setprio 0
	s_setprio 1
	v_mfma_f32_16x16x32_bf16 v[54:57], v[168:171], v[184:187], v[54:57]
	v_mfma_f32_16x16x32_bf16 v[46:49], v[176:179], v[184:187], v[46:49]
	v_mfma_f32_16x16x32_bf16 v[38:41], v[168:171], v[192:195], v[38:41]
	v_mfma_f32_16x16x32_bf16 v[30:33], v[176:179], v[192:195], v[30:33]
	v_mfma_f32_16x16x32_bf16 v[22:25], v[168:171], v[200:203], v[22:25]
	v_mfma_f32_16x16x32_bf16 v[14:17], v[176:179], v[200:203], v[14:17]
	v_mfma_f32_16x16x32_bf16 v[6:9], v[168:171], v[208:211], v[6:9]
	v_mfma_f32_16x16x32_bf16 v[2:5], v[176:179], v[208:211], v[2:5]
	v_mfma_f32_16x16x32_bf16 v[54:57], v[172:175], v[188:191], v[54:57]
	v_mfma_f32_16x16x32_bf16 v[46:49], v[180:183], v[188:191], v[46:49]
	v_mfma_f32_16x16x32_bf16 v[38:41], v[172:175], v[196:199], v[38:41]
	v_mfma_f32_16x16x32_bf16 v[30:33], v[180:183], v[196:199], v[30:33]
	v_mfma_f32_16x16x32_bf16 v[22:25], v[172:175], v[204:207], v[22:25]
	v_mfma_f32_16x16x32_bf16 v[14:17], v[180:183], v[204:207], v[14:17]
	v_mfma_f32_16x16x32_bf16 v[6:9], v[172:175], v[212:215], v[6:9]
	v_mfma_f32_16x16x32_bf16 v[2:5], v[180:183], v[212:215], v[2:5]
	s_setprio 0
	s_barrier
	s_add_i32 s72, 0, 0x18000
	s_add_i32 s73, 0, 0x1c000
	v_add_u32_e32 v164, s72, v147
	v_add_u32_e32 v180, s73, v147
	ds_read_b128 v[152:155], v164
	ds_read_b128 v[156:159], v164 offset:1024
	ds_read_b128 v[160:163], v164 offset:2048
	ds_read_b128 v[164:167], v164 offset:3072
	ds_read_b128 v[168:171], v180
	ds_read_b128 v[172:175], v180 offset:1024
	ds_read_b128 v[176:179], v180 offset:2048
	ds_read_b128 v[180:183], v180 offset:3072
	s_add_u32 s42, s42, 0x100000
	s_addc_u32 s43, s43, 0
	s_mov_b32 m0, s56
	v_lshl_add_u64 v[224:225], s[42:43], 0, v[130:131]
	ds_read_b128 v[184:187], v151 offset:32768
	ds_read_b128 v[188:191], v151 offset:33792
	ds_read_b128 v[192:195], v151 offset:34816
	ds_read_b128 v[196:199], v151 offset:35840
	ds_read_b128 v[200:203], v151 offset:36864
	ds_read_b128 v[204:207], v151 offset:37888
	ds_read_b128 v[208:211], v151 offset:38912
	ds_read_b128 v[212:215], v151 offset:39936
	global_load_lds_dwordx4 v[224:225], off
	v_lshl_add_u64 v[224:225], s[42:43], 0, v[134:135]
	s_mov_b32 m0, s57
	s_nop 0
	global_load_lds_dwordx4 v[224:225], off
	s_waitcnt vmcnt(8)
	s_waitcnt lgkmcnt(0)
	s_barrier
	s_setprio 1
	s_waitcnt lgkmcnt(0)
	v_mfma_f32_16x16x32_bf16 v[126:129], v[152:155], v[184:187], v[126:129]
	v_mfma_f32_16x16x32_bf16 v[122:125], v[160:163], v[184:187], v[122:125]
	v_mfma_f32_16x16x32_bf16 v[114:117], v[152:155], v[192:195], v[114:117]
	v_mfma_f32_16x16x32_bf16 v[106:109], v[160:163], v[192:195], v[106:109]
	v_mfma_f32_16x16x32_bf16 v[98:101], v[152:155], v[200:203], v[98:101]
	v_mfma_f32_16x16x32_bf16 v[90:93], v[160:163], v[200:203], v[90:93]
	v_mfma_f32_16x16x32_bf16 v[82:85], v[152:155], v[208:211], v[82:85]
	v_mfma_f32_16x16x32_bf16 v[74:77], v[160:163], v[208:211], v[74:77]
	v_mfma_f32_16x16x32_bf16 v[126:129], v[156:159], v[188:191], v[126:129]
	v_mfma_f32_16x16x32_bf16 v[122:125], v[164:167], v[188:191], v[122:125]
	v_mfma_f32_16x16x32_bf16 v[114:117], v[156:159], v[196:199], v[114:117]
	v_mfma_f32_16x16x32_bf16 v[106:109], v[164:167], v[196:199], v[106:109]
	v_mfma_f32_16x16x32_bf16 v[98:101], v[156:159], v[204:207], v[98:101]
	v_mfma_f32_16x16x32_bf16 v[90:93], v[164:167], v[204:207], v[90:93]
	v_mfma_f32_16x16x32_bf16 v[82:85], v[156:159], v[212:215], v[82:85]
	v_mfma_f32_16x16x32_bf16 v[74:77], v[164:167], v[212:215], v[74:77]
	s_setprio 0
	s_setprio 1
	v_mfma_f32_16x16x32_bf16 v[118:121], v[168:171], v[184:187], v[118:121]
	v_mfma_f32_16x16x32_bf16 v[110:113], v[176:179], v[184:187], v[110:113]
	v_mfma_f32_16x16x32_bf16 v[102:105], v[168:171], v[192:195], v[102:105]
	v_mfma_f32_16x16x32_bf16 v[94:97], v[176:179], v[192:195], v[94:97]
	v_mfma_f32_16x16x32_bf16 v[86:89], v[168:171], v[200:203], v[86:89]
	v_mfma_f32_16x16x32_bf16 v[78:81], v[176:179], v[200:203], v[78:81]
	v_mfma_f32_16x16x32_bf16 v[70:73], v[168:171], v[208:211], v[70:73]
	v_mfma_f32_16x16x32_bf16 v[66:69], v[176:179], v[208:211], v[66:69]
	v_mfma_f32_16x16x32_bf16 v[118:121], v[172:175], v[188:191], v[118:121]
	v_mfma_f32_16x16x32_bf16 v[110:113], v[180:183], v[188:191], v[110:113]
	v_mfma_f32_16x16x32_bf16 v[102:105], v[172:175], v[196:199], v[102:105]
	v_mfma_f32_16x16x32_bf16 v[94:97], v[180:183], v[196:199], v[94:97]
	v_mfma_f32_16x16x32_bf16 v[86:89], v[172:175], v[204:207], v[86:89]
	v_mfma_f32_16x16x32_bf16 v[78:81], v[180:183], v[204:207], v[78:81]
	v_mfma_f32_16x16x32_bf16 v[70:73], v[172:175], v[212:215], v[70:73]
	v_mfma_f32_16x16x32_bf16 v[66:69], v[180:183], v[212:215], v[66:69]
	s_setprio 0
	s_barrier
	s_add_i32 s42, s72, s54
	v_lshl_add_u64 v[216:217], v[216:217], 0, s[6:7]
	s_mov_b32 m0, s42
	ds_read_b128 v[184:187], v151 offset:49152
	ds_read_b128 v[188:191], v151 offset:50176
	ds_read_b128 v[192:195], v151 offset:51200
	ds_read_b128 v[196:199], v151 offset:52224
	ds_read_b128 v[200:203], v151 offset:53248
	ds_read_b128 v[204:207], v151 offset:54272
	ds_read_b128 v[208:211], v151 offset:55296
	ds_read_b128 v[212:215], v151 offset:56320
	global_load_lds_dwordx4 v[216:217], off
	s_add_i32 m0, s42, 0x2000
	s_add_u32 s40, s40, 0x100080
	v_lshl_add_u64 v[216:217], v[218:219], 0, s[6:7]
	s_addc_u32 s41, s41, 0
	s_add_i32 s42, s73, s54
	global_load_lds_dwordx4 v[216:217], off
	v_lshl_add_u64 v[216:217], s[40:41], 0, v[132:133]
	s_mov_b32 m0, s42
	s_nop 0
	global_load_lds_dwordx4 v[216:217], off
	v_lshl_add_u64 v[216:217], s[40:41], 0, v[136:137]
	s_add_i32 m0, s42, 0x2000
	s_nop 0
	global_load_lds_dwordx4 v[216:217], off
	v_lshl_add_u64 v[216:217], v[220:221], 0, s[6:7]
	s_mov_b32 m0, s58
	s_nop 0
	global_load_lds_dwordx4 v[216:217], off
	v_lshl_add_u64 v[216:217], v[222:223], 0, s[6:7]
	s_mov_b32 m0, s59
	s_nop 0
	global_load_lds_dwordx4 v[216:217], off
	s_waitcnt vmcnt(8)
	s_waitcnt lgkmcnt(0)
	s_barrier
	s_setprio 1
	s_waitcnt lgkmcnt(0)
	v_mfma_f32_16x16x32_bf16 v[62:65], v[152:155], v[184:187], v[62:65]
	v_mfma_f32_16x16x32_bf16 v[58:61], v[160:163], v[184:187], v[58:61]
	v_mfma_f32_16x16x32_bf16 v[50:53], v[152:155], v[192:195], v[50:53]
	v_mfma_f32_16x16x32_bf16 v[42:45], v[160:163], v[192:195], v[42:45]
	v_mfma_f32_16x16x32_bf16 v[34:37], v[152:155], v[200:203], v[34:37]
	v_mfma_f32_16x16x32_bf16 v[26:29], v[160:163], v[200:203], v[26:29]
	v_mfma_f32_16x16x32_bf16 v[18:21], v[152:155], v[208:211], v[18:21]
	v_mfma_f32_16x16x32_bf16 v[10:13], v[160:163], v[208:211], v[10:13]
	v_mfma_f32_16x16x32_bf16 v[62:65], v[156:159], v[188:191], v[62:65]
	v_mfma_f32_16x16x32_bf16 v[58:61], v[164:167], v[188:191], v[58:61]
	v_mfma_f32_16x16x32_bf16 v[50:53], v[156:159], v[196:199], v[50:53]
	v_mfma_f32_16x16x32_bf16 v[42:45], v[164:167], v[196:199], v[42:45]
	v_mfma_f32_16x16x32_bf16 v[34:37], v[156:159], v[204:207], v[34:37]
	v_mfma_f32_16x16x32_bf16 v[26:29], v[164:167], v[204:207], v[26:29]
	v_mfma_f32_16x16x32_bf16 v[18:21], v[156:159], v[212:215], v[18:21]
	v_mfma_f32_16x16x32_bf16 v[10:13], v[164:167], v[212:215], v[10:13]
	s_setprio 0
	s_setprio 1
	v_mfma_f32_16x16x32_bf16 v[54:57], v[168:171], v[184:187], v[54:57]
	v_mfma_f32_16x16x32_bf16 v[46:49], v[176:179], v[184:187], v[46:49]
	v_mfma_f32_16x16x32_bf16 v[38:41], v[168:171], v[192:195], v[38:41]
	v_mfma_f32_16x16x32_bf16 v[30:33], v[176:179], v[192:195], v[30:33]
	v_mfma_f32_16x16x32_bf16 v[22:25], v[168:171], v[200:203], v[22:25]
	v_mfma_f32_16x16x32_bf16 v[14:17], v[176:179], v[200:203], v[14:17]
	v_mfma_f32_16x16x32_bf16 v[6:9], v[168:171], v[208:211], v[6:9]
	v_mfma_f32_16x16x32_bf16 v[2:5], v[176:179], v[208:211], v[2:5]
	v_mfma_f32_16x16x32_bf16 v[54:57], v[172:175], v[188:191], v[54:57]
	v_mfma_f32_16x16x32_bf16 v[46:49], v[180:183], v[188:191], v[46:49]
	v_mfma_f32_16x16x32_bf16 v[38:41], v[172:175], v[196:199], v[38:41]
	v_mfma_f32_16x16x32_bf16 v[30:33], v[180:183], v[196:199], v[30:33]
	v_mfma_f32_16x16x32_bf16 v[22:25], v[172:175], v[204:207], v[22:25]
	v_mfma_f32_16x16x32_bf16 v[14:17], v[180:183], v[204:207], v[14:17]
	v_mfma_f32_16x16x32_bf16 v[6:9], v[172:175], v[212:215], v[6:9]
	v_mfma_f32_16x16x32_bf16 v[2:5], v[180:183], v[212:215], v[2:5]
	s_setprio 0
	s_barrier
	s_add_i32 s71, s71, 2
	s_add_u32 s38, s38, 0x100
	s_addc_u32 s39, s39, 0
	s_cmp_gt_u32 s71, 61
	s_cbranch_scc0 .LBB0_564
	s_and_b64 vcc, exec, s[10:11]
	s_cbranch_vccz .LBB0_567
	s_barrier

.LBB0_588:
	ds_read_b128 v[152:155], v149
	ds_read_b128 v[156:159], v149 offset:1024
	ds_read_b128 v[160:163], v149 offset:2048
	ds_read_b128 v[164:167], v149 offset:3072
	ds_read_b128 v[168:171], v150
	ds_read_b128 v[172:175], v150 offset:1024
	ds_read_b128 v[176:179], v150 offset:2048
	ds_read_b128 v[180:183], v150 offset:3072
	s_add_u32 s38, s30, s36
	s_addc_u32 s39, s31, s37
	s_add_u32 s40, s38, 0x100
	s_addc_u32 s41, s39, 0
	s_add_u32 s67, s64, s36
	s_addc_u32 s68, s65, s37
	s_cmp_eq_u32 s36, 0
	s_cselect_b64 s[38:39], -1, 0
	s_and_b64 s[38:39], s[34:35], s[38:39]
	s_cmpk_eq_i32 s36, 0x1f00
	v_cndmask_b32_e64 v184, 0, 1, s[38:39]
	s_cselect_b32 s41, s23, s41
	s_cselect_b32 s40, s62, s40
	v_readfirstlane_b32 s69, v184
	s_cselect_b32 s39, s21, s68
	s_cselect_b32 s38, s63, s67
	v_lshl_add_u64 v[216:217], v[142:143], 0, s[36:37]
	s_add_i32 m0, s29, 0xc000
	ds_read_b128 v[184:187], v151
	ds_read_b128 v[188:191], v151 offset:1024
	ds_read_b128 v[192:195], v151 offset:2048
	ds_read_b128 v[196:199], v151 offset:3072
	ds_read_b128 v[200:203], v151 offset:4096
	ds_read_b128 v[204:207], v151 offset:5120
	ds_read_b128 v[208:211], v151 offset:6144
	ds_read_b128 v[212:215], v151 offset:7168
	global_load_lds_dwordx4 v[216:217], off
	v_lshl_add_u64 v[216:217], v[144:145], 0, s[36:37]
	s_add_i32 m0, s29, 0xe000
	s_and_b32 s67, s69, 1
	global_load_lds_dwordx4 v[216:217], off
	s_cmp_lg_u32 s67, 0
	s_cbranch_scc1 .Lpg8r8
	s_waitcnt vmcnt(8)
	s_branch .Lpg8e8

.Lpg8e8:
	s_waitcnt lgkmcnt(0)
	s_barrier
	s_setprio 1
	s_waitcnt lgkmcnt(0)
	v_mfma_f32_16x16x32_bf16 v[126:129], v[152:155], v[184:187], v[126:129]
	v_mfma_f32_16x16x32_bf16 v[122:125], v[160:163], v[184:187], v[122:125]
	v_mfma_f32_16x16x32_bf16 v[114:117], v[152:155], v[192:195], v[114:117]
	v_mfma_f32_16x16x32_bf16 v[106:109], v[160:163], v[192:195], v[106:109]
	v_mfma_f32_16x16x32_bf16 v[98:101], v[152:155], v[200:203], v[98:101]
	v_mfma_f32_16x16x32_bf16 v[90:93], v[160:163], v[200:203], v[90:93]
	v_mfma_f32_16x16x32_bf16 v[82:85], v[152:155], v[208:211], v[82:85]
	v_mfma_f32_16x16x32_bf16 v[74:77], v[160:163], v[208:211], v[74:77]
	v_mfma_f32_16x16x32_bf16 v[126:129], v[156:159], v[188:191], v[126:129]
	v_mfma_f32_16x16x32_bf16 v[122:125], v[164:167], v[188:191], v[122:125]
	v_mfma_f32_16x16x32_bf16 v[114:117], v[156:159], v[196:199], v[114:117]
	v_mfma_f32_16x16x32_bf16 v[106:109], v[164:167], v[196:199], v[106:109]
	v_mfma_f32_16x16x32_bf16 v[98:101], v[156:159], v[204:207], v[98:101]
	v_mfma_f32_16x16x32_bf16 v[90:93], v[164:167], v[204:207], v[90:93]
	v_mfma_f32_16x16x32_bf16 v[82:85], v[156:159], v[212:215], v[82:85]
	v_mfma_f32_16x16x32_bf16 v[74:77], v[164:167], v[212:215], v[74:77]
	s_setprio 0
	s_setprio 1
	v_mfma_f32_16x16x32_bf16 v[118:121], v[168:171], v[184:187], v[118:121]
	v_mfma_f32_16x16x32_bf16 v[110:113], v[176:179], v[184:187], v[110:113]
	v_mfma_f32_16x16x32_bf16 v[102:105], v[168:171], v[192:195], v[102:105]
	v_mfma_f32_16x16x32_bf16 v[94:97], v[176:179], v[192:195], v[94:97]
	v_mfma_f32_16x16x32_bf16 v[86:89], v[168:171], v[200:203], v[86:89]
	v_mfma_f32_16x16x32_bf16 v[78:81], v[176:179], v[200:203], v[78:81]
	v_mfma_f32_16x16x32_bf16 v[70:73], v[168:171], v[208:211], v[70:73]
	v_mfma_f32_16x16x32_bf16 v[66:69], v[176:179], v[208:211], v[66:69]
	v_mfma_f32_16x16x32_bf16 v[118:121], v[172:175], v[188:191], v[118:121]
	v_mfma_f32_16x16x32_bf16 v[110:113], v[180:183], v[188:191], v[110:113]
	v_mfma_f32_16x16x32_bf16 v[102:105], v[172:175], v[196:199], v[102:105]
	v_mfma_f32_16x16x32_bf16 v[94:97], v[180:183], v[196:199], v[94:97]
	v_mfma_f32_16x16x32_bf16 v[86:89], v[172:175], v[204:207], v[86:89]
	v_mfma_f32_16x16x32_bf16 v[78:81], v[180:183], v[204:207], v[78:81]
	v_mfma_f32_16x16x32_bf16 v[70:73], v[172:175], v[212:215], v[70:73]
	v_mfma_f32_16x16x32_bf16 v[66:69], v[180:183], v[212:215], v[66:69]
	s_setprio 0
	s_barrier
	s_add_i32 s68, s93, s49
	v_lshl_add_u64 v[216:217], s[38:39], 0, v[132:133]
	s_mov_b32 m0, s68
	ds_read_b128 v[184:187], v151 offset:16384
	ds_read_b128 v[188:191], v151 offset:17408
	ds_read_b128 v[192:195], v151 offset:18432
	ds_read_b128 v[196:199], v151 offset:19456
	ds_read_b128 v[200:203], v151 offset:20480
	ds_read_b128 v[204:207], v151 offset:21504
	ds_read_b128 v[208:211], v151 offset:22528
	ds_read_b128 v[212:215], v151 offset:23552
	global_load_lds_dwordx4 v[216:217], off
	s_add_i32 m0, s68, 0x2000
	s_add_u32 s68, s38, 0x100000
	v_lshl_add_u64 v[218:219], s[38:39], 0, v[136:137]
	s_addc_u32 s69, s39, 0
	s_add_i32 s70, s55, s49
	global_load_lds_dwordx4 v[218:219], off
	v_lshl_add_u64 v[220:221], s[68:69], 0, v[132:133]
	s_mov_b32 m0, s70
	v_lshl_add_u64 v[222:223], s[40:41], 0, v[134:135]
	global_load_lds_dwordx4 v[220:221], off
	v_lshl_add_u64 v[220:221], s[68:69], 0, v[136:137]
	s_add_i32 m0, s70, 0x2000
	s_nop 0
	global_load_lds_dwordx4 v[220:221], off
	v_lshl_add_u64 v[220:221], s[40:41], 0, v[130:131]
	s_mov_b32 m0, s29
	s_nop 0
	global_load_lds_dwordx4 v[220:221], off
	s_mov_b32 m0, s50
	s_nop 0
	global_load_lds_dwordx4 v[222:223], off
	s_cmp_lg_u32 s67, 0
	s_cbranch_scc1 .Lpg8r9
	s_waitcnt vmcnt(8)
	s_branch .Lpg8e9

.Lpg8e9:
	s_waitcnt lgkmcnt(0)
	s_barrier
	s_setprio 1
	s_waitcnt lgkmcnt(0)
	v_mfma_f32_16x16x32_bf16 v[62:65], v[152:155], v[184:187], v[62:65]
	v_mfma_f32_16x16x32_bf16 v[58:61], v[160:163], v[184:187], v[58:61]
	v_mfma_f32_16x16x32_bf16 v[50:53], v[152:155], v[192:195], v[50:53]
	v_mfma_f32_16x16x32_bf16 v[42:45], v[160:163], v[192:195], v[42:45]
	v_mfma_f32_16x16x32_bf16 v[34:37], v[152:155], v[200:203], v[34:37]
	v_mfma_f32_16x16x32_bf16 v[26:29], v[160:163], v[200:203], v[26:29]
	v_mfma_f32_16x16x32_bf16 v[18:21], v[152:155], v[208:211], v[18:21]
	v_mfma_f32_16x16x32_bf16 v[10:13], v[160:163], v[208:211], v[10:13]
	v_mfma_f32_16x16x32_bf16 v[62:65], v[156:159], v[188:191], v[62:65]
	v_mfma_f32_16x16x32_bf16 v[58:61], v[164:167], v[188:191], v[58:61]
	v_mfma_f32_16x16x32_bf16 v[50:53], v[156:159], v[196:199], v[50:53]
	v_mfma_f32_16x16x32_bf16 v[42:45], v[164:167], v[196:199], v[42:45]
	v_mfma_f32_16x16x32_bf16 v[34:37], v[156:159], v[204:207], v[34:37]
	v_mfma_f32_16x16x32_bf16 v[26:29], v[164:167], v[204:207], v[26:29]
	v_mfma_f32_16x16x32_bf16 v[18:21], v[156:159], v[212:215], v[18:21]
	v_mfma_f32_16x16x32_bf16 v[10:13], v[164:167], v[212:215], v[10:13]
	s_setprio 0
	s_setprio 1
	v_mfma_f32_16x16x32_bf16 v[54:57], v[168:171], v[184:187], v[54:57]
	v_mfma_f32_16x16x32_bf16 v[46:49], v[176:179], v[184:187], v[46:49]
	v_mfma_f32_16x16x32_bf16 v[38:41], v[168:171], v[192:195], v[38:41]
	v_mfma_f32_16x16x32_bf16 v[30:33], v[176:179], v[192:195], v[30:33]
	v_mfma_f32_16x16x32_bf16 v[22:25], v[168:171], v[200:203], v[22:25]
	v_mfma_f32_16x16x32_bf16 v[14:17], v[176:179], v[200:203], v[14:17]
	v_mfma_f32_16x16x32_bf16 v[6:9], v[168:171], v[208:211], v[6:9]
	v_mfma_f32_16x16x32_bf16 v[2:5], v[176:179], v[208:211], v[2:5]
	v_mfma_f32_16x16x32_bf16 v[54:57], v[172:175], v[188:191], v[54:57]
	v_mfma_f32_16x16x32_bf16 v[46:49], v[180:183], v[188:191], v[46:49]
	v_mfma_f32_16x16x32_bf16 v[38:41], v[172:175], v[196:199], v[38:41]
	v_mfma_f32_16x16x32_bf16 v[30:33], v[180:183], v[196:199], v[30:33]
	v_mfma_f32_16x16x32_bf16 v[22:25], v[172:175], v[204:207], v[22:25]
	v_mfma_f32_16x16x32_bf16 v[14:17], v[180:183], v[204:207], v[14:17]
	v_mfma_f32_16x16x32_bf16 v[6:9], v[172:175], v[212:215], v[6:9]
	v_mfma_f32_16x16x32_bf16 v[2:5], v[180:183], v[212:215], v[2:5]
	s_setprio 0
	s_barrier
	s_add_i32 s67, 0, 0x18000
	s_add_i32 s68, 0, 0x1c000
	v_add_u32_e32 v164, s67, v147
	v_add_u32_e32 v180, s68, v147
	ds_read_b128 v[152:155], v164
	ds_read_b128 v[156:159], v164 offset:1024
	ds_read_b128 v[160:163], v164 offset:2048
	ds_read_b128 v[164:167], v164 offset:3072
	ds_read_b128 v[168:171], v180
	ds_read_b128 v[172:175], v180 offset:1024
	ds_read_b128 v[176:179], v180 offset:2048
	ds_read_b128 v[180:183], v180 offset:3072
	s_add_u32 s40, s40, 0x100000
	s_addc_u32 s41, s41, 0
	s_mov_b32 m0, s51
	v_lshl_add_u64 v[224:225], s[40:41], 0, v[130:131]
	ds_read_b128 v[184:187], v151 offset:32768
	ds_read_b128 v[188:191], v151 offset:33792
	ds_read_b128 v[192:195], v151 offset:34816
	ds_read_b128 v[196:199], v151 offset:35840
	ds_read_b128 v[200:203], v151 offset:36864
	ds_read_b128 v[204:207], v151 offset:37888
	ds_read_b128 v[208:211], v151 offset:38912
	ds_read_b128 v[212:215], v151 offset:39936
	global_load_lds_dwordx4 v[224:225], off
	v_lshl_add_u64 v[224:225], s[40:41], 0, v[134:135]
	s_mov_b32 m0, s52
	s_nop 0
	global_load_lds_dwordx4 v[224:225], off
	s_waitcnt vmcnt(8)
	s_waitcnt lgkmcnt(0)
	s_barrier
	s_setprio 1
	s_waitcnt lgkmcnt(0)
	v_mfma_f32_16x16x32_bf16 v[126:129], v[152:155], v[184:187], v[126:129]
	v_mfma_f32_16x16x32_bf16 v[122:125], v[160:163], v[184:187], v[122:125]
	v_mfma_f32_16x16x32_bf16 v[114:117], v[152:155], v[192:195], v[114:117]
	v_mfma_f32_16x16x32_bf16 v[106:109], v[160:163], v[192:195], v[106:109]
	v_mfma_f32_16x16x32_bf16 v[98:101], v[152:155], v[200:203], v[98:101]
	v_mfma_f32_16x16x32_bf16 v[90:93], v[160:163], v[200:203], v[90:93]
	v_mfma_f32_16x16x32_bf16 v[82:85], v[152:155], v[208:211], v[82:85]
	v_mfma_f32_16x16x32_bf16 v[74:77], v[160:163], v[208:211], v[74:77]
	v_mfma_f32_16x16x32_bf16 v[126:129], v[156:159], v[188:191], v[126:129]
	v_mfma_f32_16x16x32_bf16 v[122:125], v[164:167], v[188:191], v[122:125]
	v_mfma_f32_16x16x32_bf16 v[114:117], v[156:159], v[196:199], v[114:117]
	v_mfma_f32_16x16x32_bf16 v[106:109], v[164:167], v[196:199], v[106:109]
	v_mfma_f32_16x16x32_bf16 v[98:101], v[156:159], v[204:207], v[98:101]
	v_mfma_f32_16x16x32_bf16 v[90:93], v[164:167], v[204:207], v[90:93]
	v_mfma_f32_16x16x32_bf16 v[82:85], v[156:159], v[212:215], v[82:85]
	v_mfma_f32_16x16x32_bf16 v[74:77], v[164:167], v[212:215], v[74:77]
	s_setprio 0
	s_setprio 1
	v_mfma_f32_16x16x32_bf16 v[118:121], v[168:171], v[184:187], v[118:121]
	v_mfma_f32_16x16x32_bf16 v[110:113], v[176:179], v[184:187], v[110:113]
	v_mfma_f32_16x16x32_bf16 v[102:105], v[168:171], v[192:195], v[102:105]
	v_mfma_f32_16x16x32_bf16 v[94:97], v[176:179], v[192:195], v[94:97]
	v_mfma_f32_16x16x32_bf16 v[86:89], v[168:171], v[200:203], v[86:89]
	v_mfma_f32_16x16x32_bf16 v[78:81], v[176:179], v[200:203], v[78:81]
	v_mfma_f32_16x16x32_bf16 v[70:73], v[168:171], v[208:211], v[70:73]
	v_mfma_f32_16x16x32_bf16 v[66:69], v[176:179], v[208:211], v[66:69]
	v_mfma_f32_16x16x32_bf16 v[118:121], v[172:175], v[188:191], v[118:121]
	v_mfma_f32_16x16x32_bf16 v[110:113], v[180:183], v[188:191], v[110:113]
	v_mfma_f32_16x16x32_bf16 v[102:105], v[172:175], v[196:199], v[102:105]
	v_mfma_f32_16x16x32_bf16 v[94:97], v[180:183], v[196:199], v[94:97]
	v_mfma_f32_16x16x32_bf16 v[86:89], v[172:175], v[204:207], v[86:89]
	v_mfma_f32_16x16x32_bf16 v[78:81], v[180:183], v[204:207], v[78:81]
	v_mfma_f32_16x16x32_bf16 v[70:73], v[172:175], v[212:215], v[70:73]
	v_mfma_f32_16x16x32_bf16 v[66:69], v[180:183], v[212:215], v[66:69]
	s_setprio 0
	s_barrier
	s_add_i32 s40, s67, s49
	v_lshl_add_u64 v[216:217], v[216:217], 0, s[4:5]
	s_mov_b32 m0, s40
	ds_read_b128 v[184:187], v151 offset:49152
	ds_read_b128 v[188:191], v151 offset:50176
	ds_read_b128 v[192:195], v151 offset:51200
	ds_read_b128 v[196:199], v151 offset:52224
	ds_read_b128 v[200:203], v151 offset:53248
	ds_read_b128 v[204:207], v151 offset:54272
	ds_read_b128 v[208:211], v151 offset:55296
	ds_read_b128 v[212:215], v151 offset:56320
	global_load_lds_dwordx4 v[216:217], off
	s_add_i32 m0, s40, 0x2000
	s_add_u32 s38, s38, 0x100080
	v_lshl_add_u64 v[216:217], v[218:219], 0, s[4:5]
	s_addc_u32 s39, s39, 0
	s_add_i32 s40, s68, s49
	global_load_lds_dwordx4 v[216:217], off
	v_lshl_add_u64 v[216:217], s[38:39], 0, v[132:133]
	s_mov_b32 m0, s40
	s_nop 0
	global_load_lds_dwordx4 v[216:217], off
	v_lshl_add_u64 v[216:217], s[38:39], 0, v[136:137]
	s_add_i32 m0, s40, 0x2000
	s_nop 0
	global_load_lds_dwordx4 v[216:217], off
	v_lshl_add_u64 v[216:217], v[220:221], 0, s[4:5]
	s_mov_b32 m0, s53
	s_nop 0
	global_load_lds_dwordx4 v[216:217], off
	v_lshl_add_u64 v[216:217], v[222:223], 0, s[4:5]
	s_mov_b32 m0, s54
	s_nop 0
	global_load_lds_dwordx4 v[216:217], off
	s_waitcnt vmcnt(8)
	s_waitcnt lgkmcnt(0)
	s_barrier
	s_setprio 1
	s_waitcnt lgkmcnt(0)
	v_mfma_f32_16x16x32_bf16 v[62:65], v[152:155], v[184:187], v[62:65]
	v_mfma_f32_16x16x32_bf16 v[58:61], v[160:163], v[184:187], v[58:61]
	v_mfma_f32_16x16x32_bf16 v[50:53], v[152:155], v[192:195], v[50:53]
	v_mfma_f32_16x16x32_bf16 v[42:45], v[160:163], v[192:195], v[42:45]
	v_mfma_f32_16x16x32_bf16 v[34:37], v[152:155], v[200:203], v[34:37]
	v_mfma_f32_16x16x32_bf16 v[26:29], v[160:163], v[200:203], v[26:29]
	v_mfma_f32_16x16x32_bf16 v[18:21], v[152:155], v[208:211], v[18:21]
	v_mfma_f32_16x16x32_bf16 v[10:13], v[160:163], v[208:211], v[10:13]
	v_mfma_f32_16x16x32_bf16 v[62:65], v[156:159], v[188:191], v[62:65]
	v_mfma_f32_16x16x32_bf16 v[58:61], v[164:167], v[188:191], v[58:61]
	v_mfma_f32_16x16x32_bf16 v[50:53], v[156:159], v[196:199], v[50:53]
	v_mfma_f32_16x16x32_bf16 v[42:45], v[164:167], v[196:199], v[42:45]
	v_mfma_f32_16x16x32_bf16 v[34:37], v[156:159], v[204:207], v[34:37]
	v_mfma_f32_16x16x32_bf16 v[26:29], v[164:167], v[204:207], v[26:29]
	v_mfma_f32_16x16x32_bf16 v[18:21], v[156:159], v[212:215], v[18:21]
	v_mfma_f32_16x16x32_bf16 v[10:13], v[164:167], v[212:215], v[10:13]
	s_setprio 0
	s_setprio 1
	v_mfma_f32_16x16x32_bf16 v[54:57], v[168:171], v[184:187], v[54:57]
	v_mfma_f32_16x16x32_bf16 v[46:49], v[176:179], v[184:187], v[46:49]
	v_mfma_f32_16x16x32_bf16 v[38:41], v[168:171], v[192:195], v[38:41]
	v_mfma_f32_16x16x32_bf16 v[30:33], v[176:179], v[192:195], v[30:33]
	v_mfma_f32_16x16x32_bf16 v[22:25], v[168:171], v[200:203], v[22:25]
	v_mfma_f32_16x16x32_bf16 v[14:17], v[176:179], v[200:203], v[14:17]
	v_mfma_f32_16x16x32_bf16 v[6:9], v[168:171], v[208:211], v[6:9]
	v_mfma_f32_16x16x32_bf16 v[2:5], v[176:179], v[208:211], v[2:5]
	v_mfma_f32_16x16x32_bf16 v[54:57], v[172:175], v[188:191], v[54:57]
	v_mfma_f32_16x16x32_bf16 v[46:49], v[180:183], v[188:191], v[46:49]
	v_mfma_f32_16x16x32_bf16 v[38:41], v[172:175], v[196:199], v[38:41]
	v_mfma_f32_16x16x32_bf16 v[30:33], v[180:183], v[196:199], v[30:33]
	v_mfma_f32_16x16x32_bf16 v[22:25], v[172:175], v[204:207], v[22:25]
	v_mfma_f32_16x16x32_bf16 v[14:17], v[180:183], v[204:207], v[14:17]
	v_mfma_f32_16x16x32_bf16 v[6:9], v[172:175], v[212:215], v[6:9]
	v_mfma_f32_16x16x32_bf16 v[2:5], v[180:183], v[212:215], v[2:5]
	s_setprio 0
	s_barrier
	s_add_i32 s66, s66, 2
	s_add_u32 s36, s36, 0x100
	s_addc_u32 s37, s37, 0
	s_cmp_gt_u32 s66, 61
	s_cbranch_scc0 .LBB0_588
	s_and_b64 vcc, exec, s[6:7]
	s_cbranch_vccz .LBB0_591
	s_barrier

.LBB0_724:
	ds_read_b128 v[156:159], v153
	ds_read_b128 v[160:163], v153 offset:1024
	ds_read_b128 v[164:167], v153 offset:2048
	ds_read_b128 v[168:171], v153 offset:3072
	ds_read_b128 v[172:175], v154
	ds_read_b128 v[176:179], v154 offset:1024
	ds_read_b128 v[180:183], v154 offset:2048
	ds_read_b128 v[184:187], v154 offset:3072
	s_add_u32 s38, s30, s36
	s_addc_u32 s39, s31, s37
	s_add_u32 s40, s38, 0x100
	s_addc_u32 s41, s39, 0
	s_add_u32 s61, s58, s36
	s_addc_u32 s62, s59, s37
	s_cmp_eq_u32 s36, 0
	s_cselect_b64 s[38:39], -1, 0
	s_and_b64 s[38:39], s[34:35], s[38:39]
	s_cmpk_eq_i32 s36, 0x700
	v_cndmask_b32_e64 v148, 0, 1, s[38:39]
	s_cselect_b32 s41, s23, s41
	s_cselect_b32 s40, s56, s40
	v_readfirstlane_b32 s63, v148
	s_cselect_b32 s39, s21, s62
	s_cselect_b32 s38, s57, s61
	v_lshl_add_u64 v[148:149], v[144:145], 0, s[36:37]
	s_add_i32 m0, s29, 0xc000
	ds_read_b128 v[188:191], v155
	ds_read_b128 v[192:195], v155 offset:1024
	ds_read_b128 v[196:199], v155 offset:2048
	ds_read_b128 v[200:203], v155 offset:3072
	ds_read_b128 v[204:207], v155 offset:4096
	ds_read_b128 v[208:211], v155 offset:5120
	ds_read_b128 v[212:215], v155 offset:6144
	ds_read_b128 v[216:219], v155 offset:7168
	global_load_lds_dwordx4 v[148:149], off
	v_lshl_add_u64 v[148:149], v[146:147], 0, s[36:37]
	s_add_i32 m0, s29, 0xe000
	s_and_b32 s61, s63, 1
	global_load_lds_dwordx4 v[148:149], off
	s_cmp_lg_u32 s61, 0
	s_cbranch_scc1 .Lpg8r10
	s_waitcnt vmcnt(8)
	s_branch .Lpg8e10

.Lpg8e10:
	s_waitcnt lgkmcnt(0)
	s_barrier
	s_setprio 1
	s_waitcnt lgkmcnt(0)
	v_mfma_f32_16x16x32_bf16 v[124:127], v[156:159], v[188:191], v[124:127]
	v_mfma_f32_16x16x32_bf16 v[120:123], v[164:167], v[188:191], v[120:123]
	v_mfma_f32_16x16x32_bf16 v[112:115], v[156:159], v[196:199], v[112:115]
	v_mfma_f32_16x16x32_bf16 v[104:107], v[164:167], v[196:199], v[104:107]
	v_mfma_f32_16x16x32_bf16 v[96:99], v[156:159], v[204:207], v[96:99]
	v_mfma_f32_16x16x32_bf16 v[88:91], v[164:167], v[204:207], v[88:91]
	v_mfma_f32_16x16x32_bf16 v[80:83], v[156:159], v[212:215], v[80:83]
	v_mfma_f32_16x16x32_bf16 v[72:75], v[164:167], v[212:215], v[72:75]
	v_mfma_f32_16x16x32_bf16 v[124:127], v[160:163], v[192:195], v[124:127]
	v_mfma_f32_16x16x32_bf16 v[120:123], v[168:171], v[192:195], v[120:123]
	v_mfma_f32_16x16x32_bf16 v[112:115], v[160:163], v[200:203], v[112:115]
	v_mfma_f32_16x16x32_bf16 v[104:107], v[168:171], v[200:203], v[104:107]
	v_mfma_f32_16x16x32_bf16 v[96:99], v[160:163], v[208:211], v[96:99]
	v_mfma_f32_16x16x32_bf16 v[88:91], v[168:171], v[208:211], v[88:91]
	v_mfma_f32_16x16x32_bf16 v[80:83], v[160:163], v[216:219], v[80:83]
	v_mfma_f32_16x16x32_bf16 v[72:75], v[168:171], v[216:219], v[72:75]
	s_setprio 0
	s_setprio 1
	v_mfma_f32_16x16x32_bf16 v[116:119], v[172:175], v[188:191], v[116:119]
	v_mfma_f32_16x16x32_bf16 v[108:111], v[180:183], v[188:191], v[108:111]
	v_mfma_f32_16x16x32_bf16 v[100:103], v[172:175], v[196:199], v[100:103]
	v_mfma_f32_16x16x32_bf16 v[92:95], v[180:183], v[196:199], v[92:95]
	v_mfma_f32_16x16x32_bf16 v[84:87], v[172:175], v[204:207], v[84:87]
	v_mfma_f32_16x16x32_bf16 v[76:79], v[180:183], v[204:207], v[76:79]
	v_mfma_f32_16x16x32_bf16 v[68:71], v[172:175], v[212:215], v[68:71]
	v_mfma_f32_16x16x32_bf16 v[64:67], v[180:183], v[212:215], v[64:67]
	v_mfma_f32_16x16x32_bf16 v[116:119], v[176:179], v[192:195], v[116:119]
	v_mfma_f32_16x16x32_bf16 v[108:111], v[184:187], v[192:195], v[108:111]
	v_mfma_f32_16x16x32_bf16 v[100:103], v[176:179], v[200:203], v[100:103]
	v_mfma_f32_16x16x32_bf16 v[92:95], v[184:187], v[200:203], v[92:95]
	v_mfma_f32_16x16x32_bf16 v[84:87], v[176:179], v[208:211], v[84:87]
	v_mfma_f32_16x16x32_bf16 v[76:79], v[184:187], v[208:211], v[76:79]
	v_mfma_f32_16x16x32_bf16 v[68:71], v[176:179], v[216:219], v[68:71]
	v_mfma_f32_16x16x32_bf16 v[64:67], v[184:187], v[216:219], v[64:67]
	s_setprio 0
	s_barrier
	s_add_i32 s62, s93, s45
	v_lshl_add_u64 v[148:149], s[38:39], 0, v[130:131]
	s_mov_b32 m0, s62
	ds_read_b128 v[188:191], v155 offset:16384
	ds_read_b128 v[192:195], v155 offset:17408
	ds_read_b128 v[196:199], v155 offset:18432
	ds_read_b128 v[200:203], v155 offset:19456
	ds_read_b128 v[204:207], v155 offset:20480
	ds_read_b128 v[208:211], v155 offset:21504
	ds_read_b128 v[212:215], v155 offset:22528
	ds_read_b128 v[216:219], v155 offset:23552
	global_load_lds_dwordx4 v[148:149], off
	s_add_i32 m0, s62, 0x2000
	s_add_u32 s62, s38, 0x40000
	v_lshl_add_u64 v[220:221], s[38:39], 0, v[134:135]
	s_addc_u32 s63, s39, 0
	s_add_i32 s64, s53, s45
	global_load_lds_dwordx4 v[220:221], off
	v_lshl_add_u64 v[222:223], s[62:63], 0, v[130:131]
	s_mov_b32 m0, s64
	v_lshl_add_u64 v[224:225], s[40:41], 0, v[132:133]
	global_load_lds_dwordx4 v[222:223], off
	v_lshl_add_u64 v[222:223], s[62:63], 0, v[134:135]
	s_add_i32 m0, s64, 0x2000
	s_nop 0
	global_load_lds_dwordx4 v[222:223], off
	v_lshl_add_u64 v[222:223], s[40:41], 0, v[128:129]
	s_mov_b32 m0, s29
	s_nop 0
	global_load_lds_dwordx4 v[222:223], off
	s_mov_b32 m0, s48
	s_nop 0
	global_load_lds_dwordx4 v[224:225], off
	s_cmp_lg_u32 s61, 0
	s_cbranch_scc1 .Lpg8r11
	s_waitcnt vmcnt(8)
	s_branch .Lpg8e11

.Lpg8e11:
	s_waitcnt lgkmcnt(0)
	s_barrier
	s_setprio 1
	s_waitcnt lgkmcnt(0)
	v_mfma_f32_16x16x32_bf16 v[60:63], v[156:159], v[188:191], v[60:63]
	v_mfma_f32_16x16x32_bf16 v[56:59], v[164:167], v[188:191], v[56:59]
	v_mfma_f32_16x16x32_bf16 v[48:51], v[156:159], v[196:199], v[48:51]
	v_mfma_f32_16x16x32_bf16 v[40:43], v[164:167], v[196:199], v[40:43]
	v_mfma_f32_16x16x32_bf16 v[32:35], v[156:159], v[204:207], v[32:35]
	v_mfma_f32_16x16x32_bf16 v[24:27], v[164:167], v[204:207], v[24:27]
	v_mfma_f32_16x16x32_bf16 v[16:19], v[156:159], v[212:215], v[16:19]
	v_mfma_f32_16x16x32_bf16 v[8:11], v[164:167], v[212:215], v[8:11]
	v_mfma_f32_16x16x32_bf16 v[60:63], v[160:163], v[192:195], v[60:63]
	v_mfma_f32_16x16x32_bf16 v[56:59], v[168:171], v[192:195], v[56:59]
	v_mfma_f32_16x16x32_bf16 v[48:51], v[160:163], v[200:203], v[48:51]
	v_mfma_f32_16x16x32_bf16 v[40:43], v[168:171], v[200:203], v[40:43]
	v_mfma_f32_16x16x32_bf16 v[32:35], v[160:163], v[208:211], v[32:35]
	v_mfma_f32_16x16x32_bf16 v[24:27], v[168:171], v[208:211], v[24:27]
	v_mfma_f32_16x16x32_bf16 v[16:19], v[160:163], v[216:219], v[16:19]
	v_mfma_f32_16x16x32_bf16 v[8:11], v[168:171], v[216:219], v[8:11]
	s_setprio 0
	s_setprio 1
	v_mfma_f32_16x16x32_bf16 v[52:55], v[172:175], v[188:191], v[52:55]
	v_mfma_f32_16x16x32_bf16 v[44:47], v[180:183], v[188:191], v[44:47]
	v_mfma_f32_16x16x32_bf16 v[36:39], v[172:175], v[196:199], v[36:39]
	v_mfma_f32_16x16x32_bf16 v[28:31], v[180:183], v[196:199], v[28:31]
	v_mfma_f32_16x16x32_bf16 v[20:23], v[172:175], v[204:207], v[20:23]
	v_mfma_f32_16x16x32_bf16 v[12:15], v[180:183], v[204:207], v[12:15]
	v_mfma_f32_16x16x32_bf16 v[4:7], v[172:175], v[212:215], v[4:7]
	v_mfma_f32_16x16x32_bf16 v[0:3], v[180:183], v[212:215], v[0:3]
	v_mfma_f32_16x16x32_bf16 v[52:55], v[176:179], v[192:195], v[52:55]
	v_mfma_f32_16x16x32_bf16 v[44:47], v[184:187], v[192:195], v[44:47]
	v_mfma_f32_16x16x32_bf16 v[36:39], v[176:179], v[200:203], v[36:39]
	v_mfma_f32_16x16x32_bf16 v[28:31], v[184:187], v[200:203], v[28:31]
	v_mfma_f32_16x16x32_bf16 v[20:23], v[176:179], v[208:211], v[20:23]
	v_mfma_f32_16x16x32_bf16 v[12:15], v[184:187], v[208:211], v[12:15]
	v_mfma_f32_16x16x32_bf16 v[4:7], v[176:179], v[216:219], v[4:7]
	v_mfma_f32_16x16x32_bf16 v[0:3], v[184:187], v[216:219], v[0:3]
	s_setprio 0
	s_barrier
	s_add_i32 s61, 0, 0x18000
	s_add_i32 s62, 0, 0x1c000
	v_add_u32_e32 v168, s61, v151
	v_add_u32_e32 v184, s62, v151
	ds_read_b128 v[156:159], v168
	ds_read_b128 v[160:163], v168 offset:1024
	ds_read_b128 v[164:167], v168 offset:2048
	ds_read_b128 v[168:171], v168 offset:3072
	ds_read_b128 v[172:175], v184
	ds_read_b128 v[176:179], v184 offset:1024
	ds_read_b128 v[180:183], v184 offset:2048
	ds_read_b128 v[184:187], v184 offset:3072
	s_add_u32 s40, s40, 0x40000
	s_addc_u32 s41, s41, 0
	s_mov_b32 m0, s49
	v_lshl_add_u64 v[226:227], s[40:41], 0, v[128:129]
	ds_read_b128 v[188:191], v155 offset:32768
	ds_read_b128 v[192:195], v155 offset:33792
	ds_read_b128 v[196:199], v155 offset:34816
	ds_read_b128 v[200:203], v155 offset:35840
	ds_read_b128 v[204:207], v155 offset:36864
	ds_read_b128 v[208:211], v155 offset:37888
	ds_read_b128 v[212:215], v155 offset:38912
	ds_read_b128 v[216:219], v155 offset:39936
	global_load_lds_dwordx4 v[226:227], off
	v_lshl_add_u64 v[226:227], s[40:41], 0, v[132:133]
	s_mov_b32 m0, s50
	s_nop 0
	global_load_lds_dwordx4 v[226:227], off
	s_waitcnt vmcnt(8)
	s_waitcnt lgkmcnt(0)
	s_barrier
	s_setprio 1
	s_waitcnt lgkmcnt(0)
	v_mfma_f32_16x16x32_bf16 v[124:127], v[156:159], v[188:191], v[124:127]
	v_mfma_f32_16x16x32_bf16 v[120:123], v[164:167], v[188:191], v[120:123]
	v_mfma_f32_16x16x32_bf16 v[112:115], v[156:159], v[196:199], v[112:115]
	v_mfma_f32_16x16x32_bf16 v[104:107], v[164:167], v[196:199], v[104:107]
	v_mfma_f32_16x16x32_bf16 v[96:99], v[156:159], v[204:207], v[96:99]
	v_mfma_f32_16x16x32_bf16 v[88:91], v[164:167], v[204:207], v[88:91]
	v_mfma_f32_16x16x32_bf16 v[80:83], v[156:159], v[212:215], v[80:83]
	v_mfma_f32_16x16x32_bf16 v[72:75], v[164:167], v[212:215], v[72:75]
	v_mfma_f32_16x16x32_bf16 v[124:127], v[160:163], v[192:195], v[124:127]
	v_mfma_f32_16x16x32_bf16 v[120:123], v[168:171], v[192:195], v[120:123]
	v_mfma_f32_16x16x32_bf16 v[112:115], v[160:163], v[200:203], v[112:115]
	v_mfma_f32_16x16x32_bf16 v[104:107], v[168:171], v[200:203], v[104:107]
	v_mfma_f32_16x16x32_bf16 v[96:99], v[160:163], v[208:211], v[96:99]
	v_mfma_f32_16x16x32_bf16 v[88:91], v[168:171], v[208:211], v[88:91]
	v_mfma_f32_16x16x32_bf16 v[80:83], v[160:163], v[216:219], v[80:83]
	v_mfma_f32_16x16x32_bf16 v[72:75], v[168:171], v[216:219], v[72:75]
	s_setprio 0
	s_setprio 1
	v_mfma_f32_16x16x32_bf16 v[116:119], v[172:175], v[188:191], v[116:119]
	v_mfma_f32_16x16x32_bf16 v[108:111], v[180:183], v[188:191], v[108:111]
	v_mfma_f32_16x16x32_bf16 v[100:103], v[172:175], v[196:199], v[100:103]
	v_mfma_f32_16x16x32_bf16 v[92:95], v[180:183], v[196:199], v[92:95]
	v_mfma_f32_16x16x32_bf16 v[84:87], v[172:175], v[204:207], v[84:87]
	v_mfma_f32_16x16x32_bf16 v[76:79], v[180:183], v[204:207], v[76:79]
	v_mfma_f32_16x16x32_bf16 v[68:71], v[172:175], v[212:215], v[68:71]
	v_mfma_f32_16x16x32_bf16 v[64:67], v[180:183], v[212:215], v[64:67]
	v_mfma_f32_16x16x32_bf16 v[116:119], v[176:179], v[192:195], v[116:119]
	v_mfma_f32_16x16x32_bf16 v[108:111], v[184:187], v[192:195], v[108:111]
	v_mfma_f32_16x16x32_bf16 v[100:103], v[176:179], v[200:203], v[100:103]
	v_mfma_f32_16x16x32_bf16 v[92:95], v[184:187], v[200:203], v[92:95]
	v_mfma_f32_16x16x32_bf16 v[84:87], v[176:179], v[208:211], v[84:87]
	v_mfma_f32_16x16x32_bf16 v[76:79], v[184:187], v[208:211], v[76:79]
	v_mfma_f32_16x16x32_bf16 v[68:71], v[176:179], v[216:219], v[68:71]
	v_mfma_f32_16x16x32_bf16 v[64:67], v[184:187], v[216:219], v[64:67]
	s_setprio 0
	s_barrier
	s_add_i32 s40, s61, s45
	v_lshl_add_u64 v[148:149], v[148:149], 0, s[8:9]
	s_mov_b32 m0, s40
	ds_read_b128 v[188:191], v155 offset:49152
	ds_read_b128 v[192:195], v155 offset:50176
	ds_read_b128 v[196:199], v155 offset:51200
	ds_read_b128 v[200:203], v155 offset:52224
	ds_read_b128 v[204:207], v155 offset:53248
	ds_read_b128 v[208:211], v155 offset:54272
	ds_read_b128 v[212:215], v155 offset:55296
	ds_read_b128 v[216:219], v155 offset:56320
	global_load_lds_dwordx4 v[148:149], off
	s_add_i32 m0, s40, 0x2000
	s_add_u32 s38, s38, 0x40080
	v_lshl_add_u64 v[148:149], v[220:221], 0, s[8:9]
	s_addc_u32 s39, s39, 0
	s_add_i32 s40, s62, s45
	global_load_lds_dwordx4 v[148:149], off
	v_lshl_add_u64 v[148:149], s[38:39], 0, v[130:131]
	s_mov_b32 m0, s40
	s_nop 0
	global_load_lds_dwordx4 v[148:149], off
	v_lshl_add_u64 v[148:149], s[38:39], 0, v[134:135]
	s_add_i32 m0, s40, 0x2000
	s_nop 0
	global_load_lds_dwordx4 v[148:149], off
	v_lshl_add_u64 v[148:149], v[222:223], 0, s[8:9]
	s_mov_b32 m0, s51
	s_nop 0
	global_load_lds_dwordx4 v[148:149], off
	v_lshl_add_u64 v[148:149], v[224:225], 0, s[8:9]
	s_mov_b32 m0, s52
	s_nop 0
	global_load_lds_dwordx4 v[148:149], off
	s_waitcnt vmcnt(8)
	s_waitcnt lgkmcnt(0)
	s_barrier
	s_setprio 1
	s_waitcnt lgkmcnt(0)
	v_mfma_f32_16x16x32_bf16 v[60:63], v[156:159], v[188:191], v[60:63]
	v_mfma_f32_16x16x32_bf16 v[56:59], v[164:167], v[188:191], v[56:59]
	v_mfma_f32_16x16x32_bf16 v[48:51], v[156:159], v[196:199], v[48:51]
	v_mfma_f32_16x16x32_bf16 v[40:43], v[164:167], v[196:199], v[40:43]
	v_mfma_f32_16x16x32_bf16 v[32:35], v[156:159], v[204:207], v[32:35]
	v_mfma_f32_16x16x32_bf16 v[24:27], v[164:167], v[204:207], v[24:27]
	v_mfma_f32_16x16x32_bf16 v[16:19], v[156:159], v[212:215], v[16:19]
	v_mfma_f32_16x16x32_bf16 v[8:11], v[164:167], v[212:215], v[8:11]
	v_mfma_f32_16x16x32_bf16 v[60:63], v[160:163], v[192:195], v[60:63]
	v_mfma_f32_16x16x32_bf16 v[56:59], v[168:171], v[192:195], v[56:59]
	v_mfma_f32_16x16x32_bf16 v[48:51], v[160:163], v[200:203], v[48:51]
	v_mfma_f32_16x16x32_bf16 v[40:43], v[168:171], v[200:203], v[40:43]
	v_mfma_f32_16x16x32_bf16 v[32:35], v[160:163], v[208:211], v[32:35]
	v_mfma_f32_16x16x32_bf16 v[24:27], v[168:171], v[208:211], v[24:27]
	v_mfma_f32_16x16x32_bf16 v[16:19], v[160:163], v[216:219], v[16:19]
	v_mfma_f32_16x16x32_bf16 v[8:11], v[168:171], v[216:219], v[8:11]
	s_setprio 0
	s_setprio 1
	v_mfma_f32_16x16x32_bf16 v[52:55], v[172:175], v[188:191], v[52:55]
	v_mfma_f32_16x16x32_bf16 v[44:47], v[180:183], v[188:191], v[44:47]
	v_mfma_f32_16x16x32_bf16 v[36:39], v[172:175], v[196:199], v[36:39]
	v_mfma_f32_16x16x32_bf16 v[28:31], v[180:183], v[196:199], v[28:31]
	v_mfma_f32_16x16x32_bf16 v[20:23], v[172:175], v[204:207], v[20:23]
	v_mfma_f32_16x16x32_bf16 v[12:15], v[180:183], v[204:207], v[12:15]
	v_mfma_f32_16x16x32_bf16 v[4:7], v[172:175], v[212:215], v[4:7]
	v_mfma_f32_16x16x32_bf16 v[0:3], v[180:183], v[212:215], v[0:3]
	v_mfma_f32_16x16x32_bf16 v[52:55], v[176:179], v[192:195], v[52:55]
	v_mfma_f32_16x16x32_bf16 v[44:47], v[184:187], v[192:195], v[44:47]
	v_mfma_f32_16x16x32_bf16 v[36:39], v[176:179], v[200:203], v[36:39]
	v_mfma_f32_16x16x32_bf16 v[28:31], v[184:187], v[200:203], v[28:31]
	v_mfma_f32_16x16x32_bf16 v[20:23], v[176:179], v[208:211], v[20:23]
	v_mfma_f32_16x16x32_bf16 v[12:15], v[184:187], v[208:211], v[12:15]
	v_mfma_f32_16x16x32_bf16 v[4:7], v[176:179], v[216:219], v[4:7]
	v_mfma_f32_16x16x32_bf16 v[0:3], v[184:187], v[216:219], v[0:3]
	s_setprio 0
	s_barrier
	s_add_i32 s60, s60, 2
	s_add_u32 s36, s36, 0x100
	s_addc_u32 s37, s37, 0
	s_cmp_gt_u32 s60, 13
	s_cbranch_scc0 .LBB0_724
	s_and_b64 vcc, exec, s[10:11]
	s_cbranch_vccz .LBB0_727
	s_barrier
